# KV-split of the second global units across WG pairs in both layers (partner does tiles 244-260 in layer 0, 220-260 in layer 1, after its own unit), modvec weight-row loads 6 rows in flight
# speedup vs baseline: 1.0449x; 1.0043x over previous
_Z6mk_fwd5FArgs:
	s_mov_b32 s32, 0
	v_readfirstlane_b32 s10, v0
	v_writelane_b32 v254, s2, 0
	v_cmp_eq_u32_e64 s[4:5], 0, v0
	s_mov_b64 s[2:3], exec
	s_nop 0
	v_writelane_b32 v254, s4, 1
	s_nop 1
	v_writelane_b32 v254, s5, 2
	s_and_b64 s[4:5], s[2:3], s[4:5]
	s_mov_b64 exec, s[4:5]
	s_cbranch_execz .LBB0_2
	s_add_i32 s4, 0, 0x26000
	v_mov_b32_e32 v2, 0
	v_mov_b32_e32 v3, v2
	v_mov_b32_e32 v4, v2
	v_mov_b32_e32 v5, v2
	v_mov_b32_e32 v1, s4
	ds_write_b128 v1, v[2:5]

.LBB0_580:
	s_or_b64 exec, exec, s[34:35]
	v_readlane_b32 s0, v254, 31
	v_mov_b32_e32 v0, 0x26400
	v_readlane_b32 s1, v254, 32
	s_waitcnt lgkmcnt(0)
	s_barrier
	s_xor_b64 s[0:1], s[0:1], -1
	ds_read2_b32 v[0:1], v0 offset0:46 offset1:47
	v_writelane_b32 v254, s0, 37
	s_waitcnt lgkmcnt(0)
	s_nop 0
	v_writelane_b32 v254, s1, 38
	v_readfirstlane_b32 s0, v0
	v_mov_b32_e32 v0, 0x26400
	v_readfirstlane_b32 s1, v1
	ds_read2_b32 v[0:1], v0 offset0:46 offset1:47
	s_waitcnt lgkmcnt(0)
	v_writelane_b32 v254, s0, 39
	s_add_u32 s34, s0, 0x11800000
	v_readfirstlane_b32 s0, v0
	v_mov_b32_e32 v0, 0x26400
	v_writelane_b32 v254, s1, 40
	s_addc_u32 s35, s1, 0
	v_readfirstlane_b32 s1, v1
	ds_read2_b32 v[0:1], v0 offset0:18 offset1:19
	s_waitcnt lgkmcnt(0)
	v_writelane_b32 v254, s0, 41
	v_readfirstlane_b32 s12, v0
	v_mov_b32_e32 v0, 0x26400
	v_readfirstlane_b32 s13, v1
	ds_read2_b32 v[0:1], v0 offset0:24 offset1:25
	s_waitcnt lgkmcnt(0)
	s_add_u32 s0, s0, 0x2af00000
	v_readfirstlane_b32 s26, v0
	v_mov_b32_e32 v0, 0x26400
	v_readfirstlane_b32 s27, v1
	ds_read2_b32 v[0:1], v0 offset0:20 offset1:21
	s_waitcnt lgkmcnt(0)
	v_writelane_b32 v254, s0, 42
	v_readfirstlane_b32 s2, v0
	v_mov_b32_e32 v0, 0x26400
	v_readfirstlane_b32 s3, v1
	ds_read2_b32 v[0:1], v0 offset0:22 offset1:23
	s_waitcnt lgkmcnt(0)
	v_writelane_b32 v254, s1, 43
	v_readfirstlane_b32 s4, v0
	v_mov_b32_e32 v0, 0x26400
	v_readfirstlane_b32 s5, v1
	ds_read2_b32 v[0:1], v0 offset0:46 offset1:47
	s_waitcnt lgkmcnt(0)
	s_addc_u32 s0, s1, 0
	v_mov_b32_e32 v0, 0x26400
	ds_read2_b32 v[0:1], v0 offset0:46 offset1:47
	s_waitcnt lgkmcnt(0)
	v_writelane_b32 v254, s0, 44
	v_mov_b32_e32 v0, 0x26400
	ds_read_b32 v0, v0 offset:192
	s_waitcnt lgkmcnt(0)
	s_lshl_b64 s[0:1], s[30:31], 2
	v_readfirstlane_b32 s14, v0
	v_mov_b32_e32 v0, v193
	s_add_u32 s2, s2, s0
	v_mbcnt_lo_u32_b32 v0, -1, v0
	v_mbcnt_hi_u32_b32 v0, -1, v0
	v_ashrrev_i32_e32 v1, 31, v0
	s_addc_u32 s3, s3, s1
	v_lshlrev_b64 v[0:1], 2, v[0:1]
	v_lshl_add_u64 v[2:3], s[2:3], 0, v[0:1]
	global_load_dword v4, v[2:3], off
	s_nop 0
	global_load_dword v2, v[2:3], off offset:256
	s_add_u32 s0, s4, s0
	s_addc_u32 s1, s5, s1
	v_lshl_add_u64 v[0:1], s[0:1], 0, v[0:1]
	s_waitcnt vmcnt(0)
	v_max_f32_e64 v3, |v4|, |v4|
	v_max_f32_e64 v2, |v2|, |v2|
	v_max_f32_e32 v2, v3, v2
	s_nop 1
	v_mov_b32_dpp v3, v2 quad_perm:[1,0,3,2] row_mask:0xf bank_mask:0xf bound_ctrl:1
	v_max_f32_e32 v3, v3, v3
	v_max_f32_e32 v2, v2, v3
	s_nop 1
	v_mov_b32_dpp v3, v2 quad_perm:[2,3,0,1] row_mask:0xf bank_mask:0xf bound_ctrl:1
	v_max_f32_e32 v3, v3, v3
	v_max_f32_e32 v2, v2, v3
	s_nop 1
	v_mov_b32_dpp v3, v2 row_half_mirror row_mask:0xf bank_mask:0xf bound_ctrl:1
	v_max_f32_e32 v3, v3, v3
	v_max_f32_e32 v2, v2, v3
	s_nop 1
	v_mov_b32_dpp v3, v2 row_mirror row_mask:0xf bank_mask:0xf bound_ctrl:1
	v_max_f32_e32 v3, v3, v3
	v_max_f32_e32 v2, v2, v3
	ds_swizzle_b32 v3, v2 offset:swizzle(SWAP,16)
	s_waitcnt lgkmcnt(0)
	v_max_f32_e32 v3, v3, v3
	v_max_f32_e32 v2, v2, v3
	s_nop 0
	v_readlane_b32 s2, v2, 0
	v_readlane_b32 s3, v2, 32
	s_nop 0
	v_max_f32_e64 v3, s2, s2
	v_max_f32_e64 v2, s3, s3
	v_max_f32_e32 v2, v3, v2
	global_load_dword v3, v[0:1], off
	s_nop 0
	global_load_dword v0, v[0:1], off offset:256
	v_readlane_b32 s2, v254, 11
	v_readlane_b32 s3, v254, 12
	s_andn2_b64 vcc, exec, s[2:3]
	s_waitcnt vmcnt(1)
	v_max_f32_e64 v1, |v3|, |v3|
	s_waitcnt vmcnt(0)
	v_max_f32_e64 v0, |v0|, |v0|
	v_max_f32_e32 v0, v1, v0
	s_nop 1
	v_mov_b32_dpp v1, v0 quad_perm:[1,0,3,2] row_mask:0xf bank_mask:0xf bound_ctrl:1
	v_max_f32_e32 v1, v1, v1
	v_max_f32_e32 v0, v0, v1
	s_nop 1
	v_mov_b32_dpp v1, v0 quad_perm:[2,3,0,1] row_mask:0xf bank_mask:0xf bound_ctrl:1
	v_max_f32_e32 v1, v1, v1
	v_max_f32_e32 v0, v0, v1
	s_nop 1
	v_mov_b32_dpp v1, v0 row_half_mirror row_mask:0xf bank_mask:0xf bound_ctrl:1
	v_max_f32_e32 v1, v1, v1
	v_max_f32_e32 v0, v0, v1
	s_nop 1
	v_mov_b32_dpp v1, v0 row_mirror row_mask:0xf bank_mask:0xf bound_ctrl:1
	v_max_f32_e32 v1, v1, v1
	v_max_f32_e32 v0, v0, v1
	ds_swizzle_b32 v1, v0 offset:swizzle(SWAP,16)
	s_waitcnt lgkmcnt(0)
	v_max_f32_e32 v1, v1, v1
	v_max_f32_e32 v0, v0, v1
	s_nop 0
	v_readlane_b32 s0, v0, 0
	v_readlane_b32 s1, v0, 32
	s_nop 0
	v_max_f32_e64 v1, s0, s0
	v_max_f32_e64 v0, s1, s1
	v_max_f32_e32 v0, v1, v0
	v_mul_f32_e32 v1, 0x43000000, v2
	v_mul_f32_e32 v0, v1, v0
	s_nop 0
	v_readfirstlane_b32 s0, v0
	s_cbranch_vccnz .LBB0_597
	v_mov_b32_e32 v0, 0x3f83d70a
	v_mul_f32_e32 v0, s0, v0
	v_mul_f32_e32 v1, 0x3e0293ee, v0
	s_mov_b32 s0, 0x42800000
	v_cmp_ge_f32_e64 s[4:5], s0, v1
	v_readlane_b32 s0, v254, 39
	s_add_u32 s15, s0, 0x11801800
	v_readlane_b32 s1, v254, 40
	s_addc_u32 s16, s1, 0
	s_add_u32 s17, s0, 0x11801a00
	v_mul_f32_e32 v176, 0xbe0293ee, v0
	s_addc_u32 s18, s1, 0
	v_mov_b32_e32 v178, v176
	v_mov_b32_e32 v179, v176
	v_mov_b32_e32 v180, v176
	v_mov_b32_e32 v181, v176
	v_readlane_b32 s19, v254, 0
	s_add_i32 s32, s32, 1
	s_mov_b32 s28, 0
	s_movk_i32 s29, 0x100
	s_mov_b32 s30, 0
	s_mov_b32 s31, 0
	s_cmpk_lg_u32 s14, 0x100
	s_cbranch_scc1 .LBB0_584
	s_cmp_eq_u64 s[4:5], 0
	s_cbranch_scc1 .LBB0_584
	s_mov_b32 s31, 1
	v_readlane_b32 s0, v254, 39
	v_readlane_b32 s1, v254, 40
	s_and_b32 s40, s19, 0x7f
	s_lshl_b32 s41, s40, 8
	s_add_u32 s36, s0, s41
	s_addc_u32 s37, s1, 0
	s_add_u32 s36, s36, 0x60000
	s_addc_u32 s37, s37, 0
	s_mul_i32 s41, s40, 0x20800
	s_add_u32 s38, s0, s41
	s_addc_u32 s39, s1, 0
	s_add_u32 s38, s38, 0x35000000
	s_addc_u32 s39, s39, 0
	s_branch .LBB0_584

.LBB0_583:
	s_cmp_lg_u32 s31, 0
	s_cbranch_scc1 .Lkv_latch
	s_add_i32 s19, s19, s14
	s_cmpk_gt_i32 s19, 0x17f
	s_cbranch_scc1 .LBB0_597
.LBB0_584:
	v_mov_b32_e32 v0, v193
	v_readlane_b32 s0, v254, 6
	v_mbcnt_lo_u32_b32 v0, -1, v0
	v_mbcnt_hi_u32_b32 v0, -1, v0
	v_add_u32_e32 v203, s0, v0
	s_mul_hi_i32 s0, s19, 0x2aaaaaab
	s_lshr_b32 s1, s0, 31
	s_add_i32 s0, s0, s1
	s_mul_i32 s1, s0, 6
	v_cndmask_b32_e64 v0, 0, 1, s[4:5]
	s_sub_i32 s2, s19, s1
	s_lshl_b32 s10, s0, 8
	v_readfirstlane_b32 s1, v0
	s_and_b32 s24, s1, 1
	s_ashr_i32 s11, s10, 31
	s_mul_i32 s0, s0, 0x240000
	s_mul_hi_i32 s1, s10, 0x2400
	s_add_u32 s3, s34, s0
	s_addc_u32 s6, s35, s1
	s_lshl_b32 s0, s2, 7
	s_ashr_i32 s1, s0, 31
	s_lshl_b64 s[0:1], s[0:1], 1
	s_add_u32 s3, s3, s0
	s_addc_u32 s6, s6, s1
	s_add_u32 s22, s3, 0x1200
	s_mulk_i32 s2, 0x56
	s_addc_u32 s23, s6, 0
	s_bfe_u32 s3, s2, 0x1000f
	s_bfe_u32 s2, s2, 0x80008
	s_add_i32 s2, s2, s3
	s_sext_i32_i8 s2, s2
	s_lshl_b32 s2, s2, 7
	s_ashr_i32 s3, s2, 31
	s_lshl_b64 s[2:3], s[2:3], 1
	s_add_u32 s2, s2, s28
	s_addc_u32 s3, s3, 0
	s_add_u32 s6, s15, s2
	s_addc_u32 s7, s16, s3
	s_add_u32 s8, s17, s2
	s_addc_u32 s9, s18, s3
	s_lshl_b64 s[10:11], s[10:11], 12
	v_readlane_b32 s20, v254, 42
	v_ashrrev_i32_e32 v0, 1, v203
	s_add_u32 s20, s20, s10
	v_readlane_b32 s10, v254, 44
	v_bfe_u32 v201, v203, 5, 1
	v_and_b32_e32 v182, 0xffffffe0, v0
	v_bfi_b32 v2, s67, v0, v203
	v_mov_b64_e32 v[0:1], s[22:23]
	s_addc_u32 s21, s10, s11
	v_mad_i64_i32 v[0:1], s[10:11], v2, s66, v[0:1]
	v_lshlrev_b32_e32 v184, 4, v201
	v_mov_b32_e32 v185, v193
	v_lshl_add_u64 v[150:151], v[0:1], 0, v[184:185]
	v_ashrrev_i32_e32 v0, 4, v203
	v_add_u32_e32 v7, 32, v0
	v_and_b32_e32 v3, 0xfffff0, v0
	v_lshlrev_b32_e32 v4, 1, v0
	v_and_b32_e32 v8, 0xfffff0, v7
	v_lshlrev_b32_e32 v9, 1, v7
	v_lshlrev_b32_e32 v1, 3, v203
	v_and_or_b32 v3, v4, 8, v3
	v_and_or_b32 v8, v9, 8, v8
	v_and_b32_e32 v2, 0x78, v1
	v_lshrrev_b32_e32 v4, 1, v0
	v_lshrrev_b32_e32 v3, 1, v3
	v_bfe_u32 v1, v1, 5, 2
	v_and_b32_e32 v5, 3, v0
	v_lshrrev_b32_e32 v8, 1, v8
	v_or_b32_e32 v3, v3, v1
	v_and_or_b32 v4, v4, 4, v5
	v_lshlrev_b32_e32 v5, 1, v2
	v_or_b32_e32 v1, v8, v1
	v_lshlrev_b32_e32 v3, 9, v3
	v_lshlrev_b32_e32 v4, 6, v4
	v_and_b32_e32 v6, 48, v5
	v_lshlrev_b32_e32 v1, 9, v1
	v_and_b32_e32 v202, 63, v203
	v_or3_b32 v3, v3, v4, v6
	v_or3_b32 v1, v1, v4, v6
	v_lshlrev_b32_e32 v6, 4, v203
	v_lshlrev_b32_e32 v4, 3, v202
	v_and_b32_e32 v6, 0xc0, v6
	v_lshlrev_b32_e32 v8, 1, v203
	v_and_or_b32 v6, v4, 24, v6
	v_and_b32_e32 v8, 32, v8
	v_and_b32_e32 v4, 0x100, v4
	v_or3_b32 v174, v6, v8, v4
	v_mul_lo_u32 v4, v0, s68
	v_or_b32_e32 v2, v4, v2
	s_cmp_lg_u32 0, -1
	v_and_b32_e32 v200, 31, v203
	v_lshlrev_b32_e32 v192, 1, v2
	v_lshlrev_b32_e32 v2, 8, v0
	v_and_b32_e32 v4, 0xf0, v203
	v_lshlrev_b32_e32 v6, 8, v7
	s_cselect_b32 s25, 0, 0
	v_add_u32_e32 v148, 0x48000, v192
	v_mov_b32_e32 v149, v193
	v_bitop3_b32 v2, v5, v2, v4 bitop3:0xde
	v_bitop3_b32 v4, v5, v6, v4 bitop3:0xde
	v_lshlrev_b32_e32 v5, 4, v200
	v_mul_lo_u32 v0, v0, s66
	v_and_b32_e32 v6, 15, v203
	s_cmp_eq_u32 s24, 0
	v_add_u32_e32 v185, s25, v174
	v_lshl_add_u64 v[152:153], s[8:9], 0, v[192:193]
	v_lshl_add_u64 v[154:155], s[8:9], 0, v[148:149]
	v_lshl_add_u64 v[156:157], s[6:7], 0, v[192:193]
	v_lshl_add_u64 v[158:159], s[6:7], 0, v[148:149]
	s_mov_b64 s[10:11], -1
	v_lshlrev_b32_e32 v175, 8, v200
	v_add_u32_e32 v204, 0, v3
	v_add_u32_e32 v205, 0, v1
	v_add_u32_e32 v206, 0, v2
	v_add_u32_e32 v207, 0, v4
	v_and_b32_e32 v188, 0xf0, v5
	v_or_b32_e32 v211, 32, v184
	v_or_b32_e32 v210, 64, v184
	v_or_b32_e32 v209, 0x60, v184
	v_or_b32_e32 v208, 0x80, v184
	v_or_b32_e32 v191, 0xa0, v184
	v_or_b32_e32 v190, 0xc0, v184
	v_or_b32_e32 v189, 0xe0, v184
	v_lshl_or_b32 v186, v6, 4, v0
	s_cbranch_scc1 .LBB0_586
	s_and_b64 vcc, exec, s[10:11]
	s_cbranch_vccz .LBB0_583
	s_branch .LBB0_591

.LBB0_593:
	ds_read_b128 v[80:83], v212 offset:49152
	ds_read_b128 v[84:87], v212 offset:57344
	ds_read_b128 v[160:163], v211 offset:49152
	ds_read_b128 v[164:167], v211 offset:57344
	v_exp_f32_e32 v168, v72
	v_exp_f32_e32 v169, v73
	s_waitcnt lgkmcnt(3)
	v_mfma_f32_32x32x16_bf16 v[96:111], v[80:83], v[140:143], 0
	v_exp_f32_e32 v170, v74
	v_exp_f32_e32 v171, v75
	v_exp_f32_e32 v172, v76
	v_exp_f32_e32 v173, v77
	v_exp_f32_e32 v174, v78
	v_exp_f32_e32 v79, v79
	s_waitcnt lgkmcnt(2)
	v_mfma_f32_32x32x16_bf16 v[80:95], v[84:87], v[140:143], 0
	s_waitcnt lgkmcnt(1)
	v_mfma_f32_32x32x16_bf16 v[96:111], v[160:163], v[136:139], v[96:111]
	s_waitcnt lgkmcnt(0)
	v_mfma_f32_32x32x16_bf16 v[80:95], v[164:167], v[136:139], v[80:95]
	ds_read_b128 v[160:163], v210 offset:49152
	ds_read_b128 v[164:167], v210 offset:57344
	s_waitcnt lgkmcnt(1)
	v_mfma_f32_32x32x16_bf16 v[96:111], v[160:163], v[132:135], v[96:111]
	s_waitcnt lgkmcnt(0)
	v_mfma_f32_32x32x16_bf16 v[80:95], v[164:167], v[132:135], v[80:95]
	ds_read_b128 v[160:163], v209 offset:49152
	ds_read_b128 v[164:167], v209 offset:57344
	s_waitcnt lgkmcnt(1)
	v_mfma_f32_32x32x16_bf16 v[96:111], v[160:163], v[128:131], v[96:111]
	s_waitcnt lgkmcnt(0)
	v_mfma_f32_32x32x16_bf16 v[80:95], v[164:167], v[128:131], v[80:95]
	ds_read_b128 v[160:163], v208 offset:49152
	ds_read_b128 v[164:167], v208 offset:57344
	s_waitcnt lgkmcnt(1)
	v_mfma_f32_32x32x16_bf16 v[96:111], v[160:163], v[124:127], v[96:111]
	s_waitcnt lgkmcnt(0)
	v_mfma_f32_32x32x16_bf16 v[80:95], v[164:167], v[124:127], v[80:95]
	ds_read_b128 v[160:163], v213 offset:49152
	ds_read_b128 v[164:167], v213 offset:57344
	s_waitcnt lgkmcnt(1)
	v_mfma_f32_32x32x16_bf16 v[96:111], v[160:163], v[120:123], v[96:111]
	s_waitcnt lgkmcnt(0)
	v_mfma_f32_32x32x16_bf16 v[80:95], v[164:167], v[120:123], v[80:95]
	ds_read_b128 v[160:163], v214 offset:49152
	ds_read_b128 v[164:167], v214 offset:57344
	s_waitcnt lgkmcnt(1)
	v_mfma_f32_32x32x16_bf16 v[96:111], v[160:163], v[116:119], v[96:111]
	s_waitcnt lgkmcnt(0)
	v_mfma_f32_32x32x16_bf16 v[80:95], v[164:167], v[116:119], v[80:95]
	ds_read_b128 v[160:163], v215 offset:49152
	ds_read_b128 v[164:167], v215 offset:57344
	s_waitcnt lgkmcnt(1)
	v_mfma_f32_32x32x16_bf16 v[96:111], v[160:163], v[112:115], v[96:111]
	v_exp_f32_e32 v160, v64
	v_add_f32_e32 v64, v233, v231
	v_add_f32_e32 v64, v229, v64
	v_add_f32_e32 v64, v232, v64
	v_add_f32_e32 v64, v228, v64
	v_add_f32_e32 v64, v230, v64
	v_add_f32_e32 v64, v226, v64
	v_add_f32_e32 v64, v227, v64
	v_add_f32_e32 v64, v223, v64
	v_add_f32_e32 v64, v225, v64
	v_add_f32_e32 v64, v222, v64
	v_add_f32_e32 v64, v224, v64
	v_add_f32_e32 v64, v188, v64
	v_exp_f32_e32 v161, v65
	v_add_f32_e32 v64, v191, v64
	v_exp_f32_e32 v162, v66
	v_add_f32_e32 v64, v189, v64
	v_exp_f32_e32 v163, v67
	v_add_f32_e32 v64, v190, v64
	s_waitcnt lgkmcnt(0)
	v_mfma_f32_32x32x16_bf16 v[80:95], v[164:167], v[112:115], v[80:95]
	v_exp_f32_e32 v164, v68
	v_add_f32_e32 v64, v160, v64
	v_exp_f32_e32 v165, v69
	v_add_f32_e32 v64, v161, v64
	v_exp_f32_e32 v166, v70
	v_add_f32_e32 v64, v162, v64
	v_exp_f32_e32 v167, v71
	v_add_f32_e32 v64, v163, v64
	v_add_f32_e32 v64, v164, v64
	v_add_f32_e32 v64, v165, v64
	v_add_f32_e32 v64, v166, v64
	v_add_f32_e32 v64, v167, v64
	v_add_f32_e32 v64, v168, v64
	v_add_f32_e32 v64, v169, v64
	v_add_f32_e32 v64, v170, v64
	v_add_f32_e32 v64, v171, v64
	v_add_f32_e32 v64, v172, v64
	v_add_f32_e32 v64, v173, v64
	v_add_f32_e32 v64, v174, v64
	v_add_f32_e32 v234, v79, v64
	v_cvt_pk_bf16_f32 v64, v231, v233
	v_cvt_pk_bf16_f32 v65, v229, v232
	v_cvt_pk_bf16_f32 v66, v228, v230
	v_cvt_pk_bf16_f32 v67, v226, v227
	v_cvt_pk_bf16_f32 v68, v223, v225
	v_cvt_pk_bf16_f32 v69, v222, v224
	v_cvt_pk_bf16_f32 v70, v188, v191
	v_cvt_pk_bf16_f32 v71, v189, v190
	v_cvt_pk_bf16_f32 v72, v160, v161
	v_cvt_pk_bf16_f32 v73, v162, v163
	v_cvt_pk_bf16_f32 v74, v164, v165
	v_cvt_pk_bf16_f32 v75, v166, v167
	v_cvt_pk_bf16_f32 v76, v168, v169
	v_cvt_pk_bf16_f32 v77, v170, v171
	v_cvt_pk_bf16_f32 v78, v172, v173
	v_cvt_pk_bf16_f32 v79, v174, v79
	s_nop 1
	v_permlane32_swap_b32_e32 v64, v66
	v_permlane32_swap_b32_e32 v65, v67
	v_permlane32_swap_b32_e32 v68, v70
	v_permlane32_swap_b32_e32 v69, v71
	v_permlane32_swap_b32_e32 v72, v74
	v_permlane32_swap_b32_e32 v73, v75
	v_permlane32_swap_b32_e32 v76, v78
	v_permlane32_swap_b32_e32 v77, v79
	v_lshl_add_u64 v[196:197], v[196:197], 0, s[100:101]
	v_lshl_add_u64 v[198:199], v[198:199], 0, s[100:101]
	global_load_dwordx4 v[160:163], v[196:197], off offset:2560
	global_load_dwordx4 v[164:167], v[196:197], off offset:2048
	global_load_dwordx4 v[172:175], v[198:199], off offset:2560
	global_load_dwordx4 v[168:171], v[198:199], off offset:2048
	ds_read_b64_tr_b16 v[222:223], v185 offset:0
	ds_read_b64_tr_b16 v[224:225], v185 offset:0x800
	ds_read_b64_tr_b16 v[226:227], v185 offset:0x1000
	ds_read_b64_tr_b16 v[228:229], v185 offset:0x1800
	ds_read_b64_tr_b16 v[230:231], v185 offset:0x2000
	ds_read_b64_tr_b16 v[232:233], v185 offset:0x2800
	ds_read_b64_tr_b16 v[236:237], v185 offset:0x3000
	ds_read_b64_tr_b16 v[238:239], v185 offset:0x3800
	s_waitcnt lgkmcnt(6)
	s_nop 0
	v_mfma_f32_32x32x16_bf16 v[0:15], v[64:67], v[222:225], v[0:15]
	ds_read_b64_tr_b16 v[222:223], v185 offset:0x200
	ds_read_b64_tr_b16 v[224:225], v185 offset:0xa00
	s_waitcnt lgkmcnt(6)
	v_mfma_f32_32x32x16_bf16 v[0:15], v[68:71], v[226:229], v[0:15]
	ds_read_b64_tr_b16 v[226:227], v185 offset:0x1200
	ds_read_b64_tr_b16 v[228:229], v185 offset:0x1a00
	s_waitcnt lgkmcnt(6)
	v_mfma_f32_32x32x16_bf16 v[0:15], v[72:75], v[230:233], v[0:15]
	ds_read_b64_tr_b16 v[230:231], v185 offset:0x2200
	ds_read_b64_tr_b16 v[232:233], v185 offset:0x2a00
	s_waitcnt lgkmcnt(6)
	v_mfma_f32_32x32x16_bf16 v[0:15], v[76:79], v[236:239], v[0:15]
	ds_read_b64_tr_b16 v[236:237], v185 offset:0x3200
	ds_read_b64_tr_b16 v[238:239], v185 offset:0x3a00
	s_waitcnt lgkmcnt(6)
	v_mfma_f32_32x32x16_bf16 v[16:31], v[64:67], v[222:225], v[16:31]
	ds_read_b64_tr_b16 v[222:223], v185 offset:0x400
	ds_read_b64_tr_b16 v[224:225], v185 offset:0xc00
	s_waitcnt lgkmcnt(6)
	v_mfma_f32_32x32x16_bf16 v[16:31], v[68:71], v[226:229], v[16:31]
	ds_read_b64_tr_b16 v[226:227], v185 offset:0x1400
	ds_read_b64_tr_b16 v[228:229], v185 offset:0x1c00
	s_waitcnt lgkmcnt(6)
	v_mfma_f32_32x32x16_bf16 v[16:31], v[72:75], v[230:233], v[16:31]
	ds_read_b64_tr_b16 v[230:231], v185 offset:0x2400
	ds_read_b64_tr_b16 v[232:233], v185 offset:0x2c00
	s_waitcnt lgkmcnt(6)
	v_mfma_f32_32x32x16_bf16 v[16:31], v[76:79], v[236:239], v[16:31]
	ds_read_b64_tr_b16 v[236:237], v185 offset:0x3400
	ds_read_b64_tr_b16 v[238:239], v185 offset:0x3c00
	s_waitcnt lgkmcnt(6)
	v_mfma_f32_32x32x16_bf16 v[32:47], v[64:67], v[222:225], v[32:47]
	ds_read_b64_tr_b16 v[222:223], v185 offset:0x600
	ds_read_b64_tr_b16 v[224:225], v185 offset:0xe00
	s_waitcnt vmcnt(4)
	ds_write_b128 v206, v[148:151] offset:32768
	ds_write_b128 v207, v[156:159] offset:32768
	s_waitcnt lgkmcnt(8)
	v_mfma_f32_32x32x16_bf16 v[32:47], v[68:71], v[226:229], v[32:47]
	ds_read_b64_tr_b16 v[226:227], v185 offset:0x1600
	ds_read_b64_tr_b16 v[228:229], v185 offset:0x1e00
	s_waitcnt lgkmcnt(8)
	v_mfma_f32_32x32x16_bf16 v[32:47], v[72:75], v[230:233], v[32:47]
	ds_read_b64_tr_b16 v[230:231], v185 offset:0x2600
	ds_read_b64_tr_b16 v[232:233], v185 offset:0x2e00
	s_waitcnt lgkmcnt(8)
	v_mfma_f32_32x32x16_bf16 v[32:47], v[76:79], v[236:239], v[32:47]
	ds_read_b64_tr_b16 v[236:237], v185 offset:0x3600
	ds_read_b64_tr_b16 v[238:239], v185 offset:0x3e00
	s_waitcnt lgkmcnt(8)
	v_mfma_f32_32x32x16_bf16 v[48:63], v[64:67], v[222:225], v[48:63]
	s_waitcnt lgkmcnt(0)
	s_barrier
	s_waitcnt vmcnt(4)
	v_exp_f32_e32 v218, v96
	v_exp_f32_e32 v219, v97
	v_exp_f32_e32 v220, v98
	v_mfma_f32_32x32x16_bf16 v[48:63], v[68:71], v[226:229], v[48:63]
	v_exp_f32_e32 v221, v99
	v_exp_f32_e32 v240, v108
	v_exp_f32_e32 v241, v109
	v_exp_f32_e32 v242, v110
	v_exp_f32_e32 v243, v111
	s_waitcnt vmcnt(7)
	ds_write_b128 v204, v[144:147]
	s_waitcnt vmcnt(6)
	ds_write_b128 v205, v[152:155]
	v_mfma_f32_32x32x16_bf16 v[48:63], v[72:75], v[230:233], v[48:63]
	v_exp_f32_e32 v230, v100
	v_exp_f32_e32 v231, v101
	v_exp_f32_e32 v232, v102
	v_exp_f32_e32 v233, v103
	v_mfma_f32_32x32x16_bf16 v[48:63], v[76:79], v[236:239], v[48:63]
	v_exp_f32_e32 v236, v104
	v_exp_f32_e32 v237, v105
	v_exp_f32_e32 v238, v106
	v_exp_f32_e32 v239, v107
	ds_read_b128 v[64:67], v212 offset:32768
	ds_read_b128 v[68:71], v212 offset:40960
	ds_read_b128 v[222:225], v211 offset:32768
	ds_read_b128 v[226:229], v211 offset:40960
	v_exp_f32_e32 v244, v86
	v_exp_f32_e32 v245, v87
	s_waitcnt lgkmcnt(3)
	v_mfma_f32_32x32x16_bf16 v[96:111], v[64:67], v[140:143], 0
	v_exp_f32_e32 v246, v88
	v_exp_f32_e32 v247, v89
	v_exp_f32_e32 v248, v90
	v_exp_f32_e32 v249, v91
	v_exp_f32_e32 v250, v92
	v_exp_f32_e32 v251, v93
	v_exp_f32_e32 v252, v94
	s_waitcnt lgkmcnt(2)
	v_mfma_f32_32x32x16_bf16 v[64:79], v[68:71], v[140:143], 0
	v_exp_f32_e32 v95, v95
	s_waitcnt lgkmcnt(1)
	v_mfma_f32_32x32x16_bf16 v[96:111], v[222:225], v[136:139], v[96:111]
	s_waitcnt lgkmcnt(0)
	v_mfma_f32_32x32x16_bf16 v[64:79], v[226:229], v[136:139], v[64:79]
	ds_read_b128 v[222:225], v210 offset:32768
	ds_read_b128 v[226:229], v210 offset:40960
	s_waitcnt lgkmcnt(1)
	v_mfma_f32_32x32x16_bf16 v[96:111], v[222:225], v[132:135], v[96:111]
	s_waitcnt lgkmcnt(0)
	v_mfma_f32_32x32x16_bf16 v[64:79], v[226:229], v[132:135], v[64:79]
	ds_read_b128 v[222:225], v209 offset:32768
	ds_read_b128 v[226:229], v209 offset:40960
	s_waitcnt lgkmcnt(1)
	v_mfma_f32_32x32x16_bf16 v[96:111], v[222:225], v[128:131], v[96:111]
	s_waitcnt lgkmcnt(0)
	v_mfma_f32_32x32x16_bf16 v[64:79], v[226:229], v[128:131], v[64:79]
	ds_read_b128 v[222:225], v208 offset:32768
	ds_read_b128 v[226:229], v208 offset:40960
	s_waitcnt lgkmcnt(1)
	v_mfma_f32_32x32x16_bf16 v[96:111], v[222:225], v[124:127], v[96:111]
	s_waitcnt lgkmcnt(0)
	v_mfma_f32_32x32x16_bf16 v[64:79], v[226:229], v[124:127], v[64:79]
	ds_read_b128 v[222:225], v213 offset:32768
	ds_read_b128 v[226:229], v213 offset:40960
	s_waitcnt lgkmcnt(1)
	v_mfma_f32_32x32x16_bf16 v[96:111], v[222:225], v[120:123], v[96:111]
	s_waitcnt lgkmcnt(0)
	v_mfma_f32_32x32x16_bf16 v[64:79], v[226:229], v[120:123], v[64:79]
	ds_read_b128 v[222:225], v214 offset:32768
	ds_read_b128 v[226:229], v214 offset:40960
	s_waitcnt lgkmcnt(1)
	v_mfma_f32_32x32x16_bf16 v[96:111], v[222:225], v[116:119], v[96:111]
	s_waitcnt lgkmcnt(0)
	v_mfma_f32_32x32x16_bf16 v[64:79], v[226:229], v[116:119], v[64:79]
	ds_read_b128 v[222:225], v215 offset:32768
	ds_read_b128 v[226:229], v215 offset:40960
	s_waitcnt lgkmcnt(1)
	v_mfma_f32_32x32x16_bf16 v[96:111], v[222:225], v[112:115], v[96:111]
	v_exp_f32_e32 v224, v80
	v_add_f32_e32 v80, v219, v218
	v_add_f32_e32 v80, v220, v80
	v_add_f32_e32 v80, v221, v80
	v_add_f32_e32 v80, v230, v80
	v_add_f32_e32 v80, v231, v80
	v_add_f32_e32 v80, v232, v80
	v_add_f32_e32 v80, v233, v80
	v_add_f32_e32 v80, v236, v80
	v_add_f32_e32 v80, v237, v80
	v_add_f32_e32 v80, v238, v80
	v_add_f32_e32 v80, v239, v80
	v_add_f32_e32 v80, v240, v80
	v_exp_f32_e32 v225, v81
	v_add_f32_e32 v80, v241, v80
	s_waitcnt lgkmcnt(0)
	v_mfma_f32_32x32x16_bf16 v[64:79], v[226:229], v[112:115], v[64:79]
	v_exp_f32_e32 v226, v82
	v_add_f32_e32 v80, v242, v80
	v_exp_f32_e32 v227, v83
	v_add_f32_e32 v80, v243, v80
	v_exp_f32_e32 v228, v84
	v_add_f32_e32 v80, v224, v80
	v_exp_f32_e32 v229, v85
	v_add_f32_e32 v80, v225, v80
	v_add_f32_e32 v80, v226, v80
	v_add_f32_e32 v80, v227, v80
	v_add_f32_e32 v80, v228, v80
	v_add_f32_e32 v80, v229, v80
	v_add_f32_e32 v80, v244, v80
	v_add_f32_e32 v80, v245, v80
	v_add_f32_e32 v80, v246, v80
	v_add_f32_e32 v80, v247, v80
	v_add_f32_e32 v80, v248, v80
	v_add_f32_e32 v80, v249, v80
	v_add_f32_e32 v80, v250, v80
	v_add_f32_e32 v80, v251, v80
	v_add_f32_e32 v80, v252, v80
	v_add_f32_e32 v222, v95, v80
	v_cvt_pk_bf16_f32 v80, v218, v219
	v_cvt_pk_bf16_f32 v81, v220, v221
	v_cvt_pk_bf16_f32 v82, v230, v231
	v_cvt_pk_bf16_f32 v83, v232, v233
	v_cvt_pk_bf16_f32 v84, v236, v237
	v_cvt_pk_bf16_f32 v85, v238, v239
	v_cvt_pk_bf16_f32 v86, v240, v241
	v_cvt_pk_bf16_f32 v87, v242, v243
	v_cvt_pk_bf16_f32 v88, v224, v225
	v_cvt_pk_bf16_f32 v89, v226, v227
	v_cvt_pk_bf16_f32 v90, v228, v229
	v_cvt_pk_bf16_f32 v91, v244, v245
	v_cvt_pk_bf16_f32 v92, v246, v247
	v_cvt_pk_bf16_f32 v93, v248, v249
	v_cvt_pk_bf16_f32 v94, v250, v251
	v_cvt_pk_bf16_f32 v95, v252, v95
	s_nop 1
	v_permlane32_swap_b32_e32 v80, v82
	v_permlane32_swap_b32_e32 v81, v83
	v_permlane32_swap_b32_e32 v84, v86
	v_permlane32_swap_b32_e32 v85, v87
	v_permlane32_swap_b32_e32 v88, v90
	v_permlane32_swap_b32_e32 v89, v91
	v_permlane32_swap_b32_e32 v92, v94
	v_permlane32_swap_b32_e32 v93, v95
	s_cmp_gt_u32 s8, s29
	s_cselect_b64 s[6:7], -1, 0
	v_lshl_add_u64 v[196:197], v[196:197], 0, s[100:101]
	v_lshl_add_u64 v[198:199], v[198:199], 0, s[100:101]
	global_load_dwordx4 v[144:147], v[196:197], off offset:2560
	global_load_dwordx4 v[148:151], v[196:197], off offset:2048
	global_load_dwordx4 v[152:155], v[198:199], off offset:2560
	global_load_dwordx4 v[156:159], v[198:199], off offset:2048
	s_branch .LBB0_592

.LBB0_595:
	s_waitcnt vmcnt(0)
	v_and_b32_e32 v80, 0x3fffffc0, v203
	s_add_i32 s2, 0, 0x10000
	v_lshl_add_u32 v144, v80, 2, s2
	ds_read_b128 v[80:83], v212 offset:49152
	ds_read_b128 v[84:87], v212 offset:57344
	v_exp_f32_e32 v65, v65
	v_exp_f32_e32 v67, v67
	s_waitcnt lgkmcnt(1)
	v_mfma_f32_32x32x16_bf16 v[96:111], v[80:83], v[140:143], 0
	s_waitcnt lgkmcnt(0)
	v_mfma_f32_32x32x16_bf16 v[80:95], v[84:87], v[140:143], 0
	ds_read_b128 v[140:143], v211 offset:49152
	ds_read_b128 v[146:149], v211 offset:57344
	s_waitcnt lgkmcnt(1)
	v_mfma_f32_32x32x16_bf16 v[96:111], v[140:143], v[136:139], v[96:111]
	s_waitcnt lgkmcnt(0)
	v_mfma_f32_32x32x16_bf16 v[80:95], v[146:149], v[136:139], v[80:95]
	ds_read_b128 v[136:139], v210 offset:49152
	ds_read_b128 v[140:143], v210 offset:57344
	s_waitcnt lgkmcnt(1)
	v_mfma_f32_32x32x16_bf16 v[96:111], v[136:139], v[132:135], v[96:111]
	s_waitcnt lgkmcnt(0)
	v_mfma_f32_32x32x16_bf16 v[80:95], v[140:143], v[132:135], v[80:95]
	ds_read_b128 v[132:135], v209 offset:49152
	ds_read_b128 v[136:139], v209 offset:57344
	s_waitcnt lgkmcnt(1)
	v_mfma_f32_32x32x16_bf16 v[96:111], v[132:135], v[128:131], v[96:111]
	s_waitcnt lgkmcnt(0)
	v_mfma_f32_32x32x16_bf16 v[80:95], v[136:139], v[128:131], v[80:95]
	ds_read_b128 v[128:131], v208 offset:49152
	ds_read_b128 v[132:135], v208 offset:57344
	s_waitcnt lgkmcnt(1)
	v_mfma_f32_32x32x16_bf16 v[96:111], v[128:131], v[124:127], v[96:111]
	s_waitcnt lgkmcnt(0)
	v_mfma_f32_32x32x16_bf16 v[80:95], v[132:135], v[124:127], v[80:95]
	ds_read_b128 v[124:127], v213 offset:49152
	ds_read_b128 v[128:131], v213 offset:57344
	s_waitcnt lgkmcnt(1)
	v_mfma_f32_32x32x16_bf16 v[96:111], v[124:127], v[120:123], v[96:111]
	s_waitcnt lgkmcnt(0)
	v_mfma_f32_32x32x16_bf16 v[80:95], v[128:131], v[120:123], v[80:95]
	ds_read_b128 v[120:123], v214 offset:49152
	ds_read_b128 v[124:127], v214 offset:57344
	s_waitcnt lgkmcnt(1)
	v_mfma_f32_32x32x16_bf16 v[96:111], v[120:123], v[116:119], v[96:111]
	s_waitcnt lgkmcnt(0)
	v_mfma_f32_32x32x16_bf16 v[80:95], v[124:127], v[116:119], v[80:95]
	ds_read_b128 v[116:119], v215 offset:49152
	ds_read_b128 v[120:123], v215 offset:57344
	v_exp_f32_e32 v124, v78
	v_exp_f32_e32 v125, v79
	s_waitcnt lgkmcnt(1)
	v_mfma_f32_32x32x16_bf16 v[96:111], v[116:119], v[112:115], v[96:111]
	v_exp_f32_e32 v116, v70
	v_exp_f32_e32 v117, v71
	v_exp_f32_e32 v118, v72
	v_exp_f32_e32 v119, v73
	s_waitcnt lgkmcnt(0)
	v_mfma_f32_32x32x16_bf16 v[80:95], v[120:123], v[112:115], v[80:95]
	v_exp_f32_e32 v112, v64
	v_add_f32_e32 v64, 0, v231
	v_add_f32_e32 v64, v233, v64
	v_add_f32_e32 v64, v229, v64
	v_add_f32_e32 v64, v232, v64
	v_add_f32_e32 v64, v228, v64
	v_add_f32_e32 v64, v230, v64
	v_add_f32_e32 v64, v226, v64
	v_add_f32_e32 v64, v227, v64
	v_add_f32_e32 v64, v223, v64
	v_add_f32_e32 v64, v225, v64
	v_add_f32_e32 v64, v222, v64
	v_add_f32_e32 v64, v224, v64
	v_add_f32_e32 v64, v188, v64
	v_add_f32_e32 v64, v191, v64
	v_exp_f32_e32 v113, v66
	v_add_f32_e32 v64, v189, v64
	v_add_f32_e32 v64, v190, v64
	v_exp_f32_e32 v114, v68
	v_add_f32_e32 v64, v112, v64
	v_exp_f32_e32 v115, v69
	v_add_f32_e32 v64, v65, v64
	v_add_f32_e32 v64, v113, v64
	v_add_f32_e32 v64, v67, v64
	v_add_f32_e32 v64, v114, v64
	v_add_f32_e32 v64, v115, v64
	v_exp_f32_e32 v120, v74
	v_add_f32_e32 v64, v116, v64
	v_exp_f32_e32 v121, v75
	v_add_f32_e32 v64, v117, v64
	v_exp_f32_e32 v122, v76
	v_add_f32_e32 v64, v118, v64
	v_exp_f32_e32 v123, v77
	v_add_f32_e32 v64, v119, v64
	v_add_f32_e32 v64, v120, v64
	v_add_f32_e32 v64, v121, v64
	v_add_f32_e32 v64, v122, v64
	v_add_f32_e32 v64, v123, v64
	v_add_f32_e32 v64, v124, v64
	v_add_f32_e32 v64, v125, v64
	v_mov_b32_e32 v66, v64
	s_nop 1
	v_permlane32_swap_b32_e32 v64, v66
	v_cvt_pk_bf16_f32 v68, v231, v233
	v_cvt_pk_bf16_f32 v69, v229, v232
	v_cvt_pk_bf16_f32 v70, v228, v230
	v_cvt_pk_bf16_f32 v71, v226, v227
	v_cvt_pk_bf16_f32 v72, v223, v225
	v_cvt_pk_bf16_f32 v73, v222, v224
	v_cvt_pk_bf16_f32 v74, v188, v191
	v_cvt_pk_bf16_f32 v75, v189, v190
	v_cvt_pk_bf16_f32 v76, v112, v65
	v_cvt_pk_bf16_f32 v77, v113, v67
	v_cvt_pk_bf16_f32 v78, v114, v115
	v_cvt_pk_bf16_f32 v79, v116, v117
	v_cvt_pk_bf16_f32 v112, v118, v119
	v_cvt_pk_bf16_f32 v113, v120, v121
	v_cvt_pk_bf16_f32 v114, v122, v123
	v_cvt_pk_bf16_f32 v115, v124, v125
	s_nop 0
	v_permlane32_swap_b32_e32 v68, v70
	v_permlane32_swap_b32_e32 v69, v71
	v_permlane32_swap_b32_e32 v72, v74
	v_permlane32_swap_b32_e32 v73, v75
	v_permlane32_swap_b32_e32 v76, v78
	v_permlane32_swap_b32_e32 v77, v79
	v_permlane32_swap_b32_e32 v112, v114
	v_permlane32_swap_b32_e32 v113, v115
	ds_read_b64_tr_b16 v[116:117], v185 offset:0
	ds_read_b64_tr_b16 v[118:119], v185 offset:0x800
	ds_read_b64_tr_b16 v[120:121], v185 offset:0x1000
	ds_read_b64_tr_b16 v[122:123], v185 offset:0x1800
	ds_read_b64_tr_b16 v[124:125], v185 offset:0x2000
	ds_read_b64_tr_b16 v[126:127], v185 offset:0x2800
	ds_read_b64_tr_b16 v[128:129], v185 offset:0x3000
	ds_read_b64_tr_b16 v[130:131], v185 offset:0x3800
	s_waitcnt lgkmcnt(0)
	s_nop 0
	v_mfma_f32_32x32x16_bf16 v[0:15], v[68:71], v[116:119], v[0:15]
	ds_read_b64_tr_b16 v[116:117], v185 offset:0x200
	ds_read_b64_tr_b16 v[118:119], v185 offset:0xa00
	v_mfma_f32_32x32x16_bf16 v[0:15], v[72:75], v[120:123], v[0:15]
	ds_read_b64_tr_b16 v[120:121], v185 offset:0x1200
	ds_read_b64_tr_b16 v[122:123], v185 offset:0x1a00
	v_mfma_f32_32x32x16_bf16 v[0:15], v[76:79], v[124:127], v[0:15]
	ds_read_b64_tr_b16 v[124:125], v185 offset:0x2200
	ds_read_b64_tr_b16 v[126:127], v185 offset:0x2a00
	v_mfma_f32_32x32x16_bf16 v[0:15], v[112:115], v[128:131], v[0:15]
	ds_read_b64_tr_b16 v[128:129], v185 offset:0x3200
	ds_read_b64_tr_b16 v[130:131], v185 offset:0x3a00
	s_waitcnt lgkmcnt(0)
	v_mfma_f32_32x32x16_bf16 v[16:31], v[68:71], v[116:119], v[16:31]
	ds_read_b64_tr_b16 v[116:117], v185 offset:0x400
	ds_read_b64_tr_b16 v[118:119], v185 offset:0xc00
	v_mfma_f32_32x32x16_bf16 v[16:31], v[72:75], v[120:123], v[16:31]
	ds_read_b64_tr_b16 v[120:121], v185 offset:0x1400
	ds_read_b64_tr_b16 v[122:123], v185 offset:0x1c00
	v_mfma_f32_32x32x16_bf16 v[16:31], v[76:79], v[124:127], v[16:31]
	ds_read_b64_tr_b16 v[124:125], v185 offset:0x2400
	ds_read_b64_tr_b16 v[126:127], v185 offset:0x2c00
	v_mfma_f32_32x32x16_bf16 v[16:31], v[112:115], v[128:131], v[16:31]
	ds_read_b64_tr_b16 v[128:129], v185 offset:0x3400
	ds_read_b64_tr_b16 v[130:131], v185 offset:0x3c00
	s_waitcnt lgkmcnt(0)
	v_mfma_f32_32x32x16_bf16 v[32:47], v[68:71], v[116:119], v[32:47]
	ds_read_b64_tr_b16 v[116:117], v185 offset:0x600
	ds_read_b64_tr_b16 v[118:119], v185 offset:0xe00
	v_mfma_f32_32x32x16_bf16 v[32:47], v[72:75], v[120:123], v[32:47]
	ds_read_b64_tr_b16 v[120:121], v185 offset:0x1600
	ds_read_b64_tr_b16 v[122:123], v185 offset:0x1e00
	v_mfma_f32_32x32x16_bf16 v[32:47], v[76:79], v[124:127], v[32:47]
	ds_read_b64_tr_b16 v[124:125], v185 offset:0x2600
	ds_read_b64_tr_b16 v[126:127], v185 offset:0x2e00
	v_mfma_f32_32x32x16_bf16 v[32:47], v[112:115], v[128:131], v[32:47]
	ds_read_b64_tr_b16 v[128:129], v185 offset:0x3600
	ds_read_b64_tr_b16 v[130:131], v185 offset:0x3e00
	s_waitcnt lgkmcnt(0)
	v_mfma_f32_32x32x16_bf16 v[48:63], v[68:71], v[116:119], v[48:63]
	v_exp_f32_e32 v68, v96
	v_exp_f32_e32 v69, v97
	v_exp_f32_e32 v70, v98
	v_exp_f32_e32 v71, v99
	v_add_f32_e32 v65, 0, v68
	v_add_f32_e32 v65, v69, v65
	v_add_f32_e32 v65, v70, v65
	v_mfma_f32_32x32x16_bf16 v[48:63], v[72:75], v[120:123], v[48:63]
	v_exp_f32_e32 v72, v100
	v_exp_f32_e32 v73, v101
	v_exp_f32_e32 v74, v102
	v_exp_f32_e32 v75, v103
	v_add_f32_e32 v65, v71, v65
	v_add_f32_e32 v65, v72, v65
	v_add_f32_e32 v65, v73, v65
	v_mfma_f32_32x32x16_bf16 v[48:63], v[76:79], v[124:127], v[48:63]
	v_exp_f32_e32 v76, v104
	v_exp_f32_e32 v77, v105
	v_exp_f32_e32 v78, v106
	v_add_f32_e32 v65, v74, v65
	v_exp_f32_e32 v79, v107
	v_add_f32_e32 v65, v75, v65
	v_exp_f32_e32 v96, v108
	v_add_f32_e32 v65, v76, v65
	v_exp_f32_e32 v97, v109
	v_add_f32_e32 v65, v77, v65
	v_exp_f32_e32 v98, v110
	v_add_f32_e32 v65, v78, v65
	v_exp_f32_e32 v99, v111
	v_add_f32_e32 v65, v79, v65
	v_exp_f32_e32 v80, v80
	v_add_f32_e32 v65, v96, v65
	v_exp_f32_e32 v81, v81
	v_add_f32_e32 v65, v97, v65
	v_exp_f32_e32 v82, v82
	v_add_f32_e32 v65, v98, v65
	v_exp_f32_e32 v83, v83
	v_add_f32_e32 v65, v99, v65
	v_exp_f32_e32 v84, v84
	v_add_f32_e32 v65, v80, v65
	v_exp_f32_e32 v85, v85
	v_add_f32_e32 v65, v81, v65
	v_exp_f32_e32 v86, v86
	v_add_f32_e32 v65, v82, v65
	v_exp_f32_e32 v87, v87
	v_add_f32_e32 v65, v83, v65
	v_exp_f32_e32 v88, v88
	v_add_f32_e32 v65, v84, v65
	v_exp_f32_e32 v89, v89
	v_add_f32_e32 v65, v85, v65
	v_exp_f32_e32 v90, v90
	v_add_f32_e32 v65, v86, v65
	v_exp_f32_e32 v91, v91
	v_add_f32_e32 v65, v87, v65
	v_exp_f32_e32 v92, v92
	v_add_f32_e32 v65, v88, v65
	v_exp_f32_e32 v93, v93
	v_add_f32_e32 v65, v89, v65
	v_mfma_f32_32x32x16_bf16 v[48:63], v[112:115], v[128:131], v[48:63]
	v_exp_f32_e32 v94, v94
	v_add_f32_e32 v65, v90, v65
	v_exp_f32_e32 v95, v95
	v_add_f32_e32 v65, v91, v65
	v_add_f32_e32 v65, v92, v65
	v_add_f32_e32 v65, v93, v65
	v_add_f32_e32 v65, v94, v65
	v_add_f32_e32 v65, v95, v65
	v_mov_b32_e32 v67, v65
	s_barrier
	s_nop 0
	v_permlane32_swap_b32_e32 v65, v67
	v_cvt_pk_bf16_f32 v68, v68, v69
	v_cvt_pk_bf16_f32 v69, v70, v71
	v_cvt_pk_bf16_f32 v70, v72, v73
	v_cvt_pk_bf16_f32 v71, v74, v75
	v_cvt_pk_bf16_f32 v72, v76, v77
	v_cvt_pk_bf16_f32 v73, v78, v79
	v_cvt_pk_bf16_f32 v74, v96, v97
	v_cvt_pk_bf16_f32 v75, v98, v99
	v_cvt_pk_bf16_f32 v76, v80, v81
	v_cvt_pk_bf16_f32 v77, v82, v83
	v_cvt_pk_bf16_f32 v78, v84, v85
	v_cvt_pk_bf16_f32 v79, v86, v87
	v_cvt_pk_bf16_f32 v80, v88, v89
	v_cvt_pk_bf16_f32 v81, v90, v91
	v_cvt_pk_bf16_f32 v82, v92, v93
	v_cvt_pk_bf16_f32 v83, v94, v95
	s_nop 0
	v_permlane32_swap_b32_e32 v68, v70
	v_permlane32_swap_b32_e32 v69, v71
	v_permlane32_swap_b32_e32 v72, v74
	v_permlane32_swap_b32_e32 v73, v75
	v_permlane32_swap_b32_e32 v76, v78
	v_permlane32_swap_b32_e32 v77, v79
	v_permlane32_swap_b32_e32 v80, v82
	v_permlane32_swap_b32_e32 v81, v83
	ds_read_b64_tr_b16 v[84:85], v177 offset:0
	ds_read_b64_tr_b16 v[86:87], v177 offset:0x800
	ds_read_b64_tr_b16 v[88:89], v177 offset:0x1000
	ds_read_b64_tr_b16 v[90:91], v177 offset:0x1800
	ds_read_b64_tr_b16 v[92:93], v177 offset:0x2000
	ds_read_b64_tr_b16 v[94:95], v177 offset:0x2800
	ds_read_b64_tr_b16 v[96:97], v177 offset:0x3000
	ds_read_b64_tr_b16 v[98:99], v177 offset:0x3800
	s_waitcnt lgkmcnt(0)
	s_nop 0
	v_mfma_f32_32x32x16_bf16 v[0:15], v[68:71], v[84:87], v[0:15]
	ds_read_b64_tr_b16 v[84:85], v177 offset:0x200
	ds_read_b64_tr_b16 v[86:87], v177 offset:0xa00
	v_mfma_f32_32x32x16_bf16 v[0:15], v[72:75], v[88:91], v[0:15]
	ds_read_b64_tr_b16 v[88:89], v177 offset:0x1200
	ds_read_b64_tr_b16 v[90:91], v177 offset:0x1a00
	v_mfma_f32_32x32x16_bf16 v[0:15], v[76:79], v[92:95], v[0:15]
	ds_read_b64_tr_b16 v[92:93], v177 offset:0x2200
	ds_read_b64_tr_b16 v[94:95], v177 offset:0x2a00
	v_mfma_f32_32x32x16_bf16 v[0:15], v[80:83], v[96:99], v[0:15]
	ds_read_b64_tr_b16 v[96:97], v177 offset:0x3200
	ds_read_b64_tr_b16 v[98:99], v177 offset:0x3a00
	s_waitcnt lgkmcnt(0)
	v_mfma_f32_32x32x16_bf16 v[16:31], v[68:71], v[84:87], v[16:31]
	ds_read_b64_tr_b16 v[84:85], v177 offset:0x400
	ds_read_b64_tr_b16 v[86:87], v177 offset:0xc00
	v_mfma_f32_32x32x16_bf16 v[16:31], v[72:75], v[88:91], v[16:31]
	ds_read_b64_tr_b16 v[88:89], v177 offset:0x1400
	ds_read_b64_tr_b16 v[90:91], v177 offset:0x1c00
	v_mfma_f32_32x32x16_bf16 v[16:31], v[76:79], v[92:95], v[16:31]
	ds_read_b64_tr_b16 v[92:93], v177 offset:0x2400
	ds_read_b64_tr_b16 v[94:95], v177 offset:0x2c00
	v_mfma_f32_32x32x16_bf16 v[16:31], v[80:83], v[96:99], v[16:31]
	ds_read_b64_tr_b16 v[96:97], v177 offset:0x3400
	ds_read_b64_tr_b16 v[98:99], v177 offset:0x3c00
	s_waitcnt lgkmcnt(0)
	v_mfma_f32_32x32x16_bf16 v[32:47], v[68:71], v[84:87], v[32:47]
	ds_read_b64_tr_b16 v[84:85], v177 offset:0x600
	ds_read_b64_tr_b16 v[86:87], v177 offset:0xe00
	v_mfma_f32_32x32x16_bf16 v[32:47], v[72:75], v[88:91], v[32:47]
	ds_read_b64_tr_b16 v[88:89], v177 offset:0x1600
	ds_read_b64_tr_b16 v[90:91], v177 offset:0x1e00
	v_mfma_f32_32x32x16_bf16 v[32:47], v[76:79], v[92:95], v[32:47]
	ds_read_b64_tr_b16 v[92:93], v177 offset:0x2600
	ds_read_b64_tr_b16 v[94:95], v177 offset:0x2e00
	v_mfma_f32_32x32x16_bf16 v[32:47], v[80:83], v[96:99], v[32:47]
	ds_read_b64_tr_b16 v[96:97], v177 offset:0x3600
	ds_read_b64_tr_b16 v[98:99], v177 offset:0x3e00
	s_waitcnt lgkmcnt(0)
	v_mfma_f32_32x32x16_bf16 v[48:63], v[68:71], v[84:87], v[48:63]
	v_cmp_gt_u32_e32 vcc, 32, v202
	v_mfma_f32_32x32x16_bf16 v[48:63], v[72:75], v[88:91], v[48:63]
	v_mfma_f32_32x32x16_bf16 v[48:63], v[76:79], v[92:95], v[48:63]
	v_mfma_f32_32x32x16_bf16 v[48:63], v[80:83], v[96:99], v[48:63]
	s_cmp_lg_u32 s30, 0
	s_cbranch_scc1 .Lkv_special
.Lkv_resume:
	s_and_saveexec_b64 s[2:3], vcc
	s_cbranch_execz .LBB0_582
	v_pk_add_f32 v[64:65], v[64:65], v[66:67]
	v_lshl_add_u32 v68, v200, 2, v144
	v_add_f32_e32 v64, v183, v64
	v_add_f32_e32 v64, v64, v65
	ds_write_b32 v68, v64
	s_branch .LBB0_582
.Lkv_latch:
	s_cmp_eq_u32 s31, 2
	s_cbranch_scc1 .LBB0_597
	s_mov_b32 s31, 2
	v_readlane_b32 s19, v254, 0
	s_nop 3
	s_cmpk_lt_u32 s19, 0x80
	s_cbranch_scc1 .Lkv_lower2
	s_add_i32 s19, s19, 0x80
	s_mov_b32 s30, 1
	s_cmp_eq_u32 s32, 1
	s_cbranch_scc1 .Lkv_upL0
	s_mov_b32 s28, 0x7bc0000
	s_movk_i32 s29, 36
	s_branch .LBB0_584
.Lkv_upL0:
	s_mov_b32 s28, 0x8940000
	s_movk_i32 s29, 12
	s_branch .LBB0_584
.Lkv_lower2:
	s_add_i32 s19, s19, 0x100
	s_mov_b32 s28, 0
	s_mov_b32 s30, 2
	s_cmp_eq_u32 s32, 1
	s_cbranch_scc1 .Lkv_loL0
	s_movk_i32 s29, 216
	s_branch .LBB0_584
.Lkv_loL0:
	s_movk_i32 s29, 240
	s_branch .LBB0_584
.Lkv_special:
	s_nop 7
	s_nop 4
	v_add_f32_e32 v64, v64, v66
	v_add_f32_e32 v65, v65, v67
	v_add_f32_e32 v64, v64, v65
	v_add_f32_e32 v64, v183, v64
	v_lshrrev_b32_e32 v68, 6, v203
	v_mul_u32_u24_e32 v68, 0x4100, v68
	v_and_b32_e32 v69, 63, v203
	v_lshl_add_u32 v68, v69, 2, v68
	s_cmp_eq_u32 s30, 2
	s_cbranch_scc1 .Lkv_merge
	global_store_dword v68, v0, s[38:39] sc0 sc1
	global_store_dword v68, v1, s[38:39] offset:256 sc0 sc1
	global_store_dword v68, v2, s[38:39] offset:512 sc0 sc1
	global_store_dword v68, v3, s[38:39] offset:768 sc0 sc1
	global_store_dword v68, v4, s[38:39] offset:1024 sc0 sc1
	global_store_dword v68, v5, s[38:39] offset:1280 sc0 sc1
	global_store_dword v68, v6, s[38:39] offset:1536 sc0 sc1
	global_store_dword v68, v7, s[38:39] offset:1792 sc0 sc1
	global_store_dword v68, v8, s[38:39] offset:2048 sc0 sc1
	global_store_dword v68, v9, s[38:39] offset:2304 sc0 sc1
	global_store_dword v68, v10, s[38:39] offset:2560 sc0 sc1
	global_store_dword v68, v11, s[38:39] offset:2816 sc0 sc1
	global_store_dword v68, v12, s[38:39] offset:3072 sc0 sc1
	global_store_dword v68, v13, s[38:39] offset:3328 sc0 sc1
	global_store_dword v68, v14, s[38:39] offset:3584 sc0 sc1
	global_store_dword v68, v15, s[38:39] offset:3840 sc0 sc1
	v_add_u32_e32 v68, 0x1000, v68
	global_store_dword v68, v16, s[38:39] sc0 sc1
	global_store_dword v68, v17, s[38:39] offset:256 sc0 sc1
	global_store_dword v68, v18, s[38:39] offset:512 sc0 sc1
	global_store_dword v68, v19, s[38:39] offset:768 sc0 sc1
	global_store_dword v68, v20, s[38:39] offset:1024 sc0 sc1
	global_store_dword v68, v21, s[38:39] offset:1280 sc0 sc1
	global_store_dword v68, v22, s[38:39] offset:1536 sc0 sc1
	global_store_dword v68, v23, s[38:39] offset:1792 sc0 sc1
	global_store_dword v68, v24, s[38:39] offset:2048 sc0 sc1
	global_store_dword v68, v25, s[38:39] offset:2304 sc0 sc1
	global_store_dword v68, v26, s[38:39] offset:2560 sc0 sc1
	global_store_dword v68, v27, s[38:39] offset:2816 sc0 sc1
	global_store_dword v68, v28, s[38:39] offset:3072 sc0 sc1
	global_store_dword v68, v29, s[38:39] offset:3328 sc0 sc1
	global_store_dword v68, v30, s[38:39] offset:3584 sc0 sc1
	global_store_dword v68, v31, s[38:39] offset:3840 sc0 sc1
	v_add_u32_e32 v68, 0x1000, v68
	global_store_dword v68, v32, s[38:39] sc0 sc1
	global_store_dword v68, v33, s[38:39] offset:256 sc0 sc1
	global_store_dword v68, v34, s[38:39] offset:512 sc0 sc1
	global_store_dword v68, v35, s[38:39] offset:768 sc0 sc1
	global_store_dword v68, v36, s[38:39] offset:1024 sc0 sc1
	global_store_dword v68, v37, s[38:39] offset:1280 sc0 sc1
	global_store_dword v68, v38, s[38:39] offset:1536 sc0 sc1
	global_store_dword v68, v39, s[38:39] offset:1792 sc0 sc1
	global_store_dword v68, v40, s[38:39] offset:2048 sc0 sc1
	global_store_dword v68, v41, s[38:39] offset:2304 sc0 sc1
	global_store_dword v68, v42, s[38:39] offset:2560 sc0 sc1
	global_store_dword v68, v43, s[38:39] offset:2816 sc0 sc1
	global_store_dword v68, v44, s[38:39] offset:3072 sc0 sc1
	global_store_dword v68, v45, s[38:39] offset:3328 sc0 sc1
	global_store_dword v68, v46, s[38:39] offset:3584 sc0 sc1
	global_store_dword v68, v47, s[38:39] offset:3840 sc0 sc1
	v_add_u32_e32 v68, 0x1000, v68
	global_store_dword v68, v48, s[38:39] sc0 sc1
	global_store_dword v68, v49, s[38:39] offset:256 sc0 sc1
	global_store_dword v68, v50, s[38:39] offset:512 sc0 sc1
	global_store_dword v68, v51, s[38:39] offset:768 sc0 sc1
	global_store_dword v68, v52, s[38:39] offset:1024 sc0 sc1
	global_store_dword v68, v53, s[38:39] offset:1280 sc0 sc1
	global_store_dword v68, v54, s[38:39] offset:1536 sc0 sc1
	global_store_dword v68, v55, s[38:39] offset:1792 sc0 sc1
	global_store_dword v68, v56, s[38:39] offset:2048 sc0 sc1
	global_store_dword v68, v57, s[38:39] offset:2304 sc0 sc1
	global_store_dword v68, v58, s[38:39] offset:2560 sc0 sc1
	global_store_dword v68, v59, s[38:39] offset:2816 sc0 sc1
	global_store_dword v68, v60, s[38:39] offset:3072 sc0 sc1
	global_store_dword v68, v61, s[38:39] offset:3328 sc0 sc1
	global_store_dword v68, v62, s[38:39] offset:3584 sc0 sc1
	global_store_dword v68, v63, s[38:39] offset:3840 sc0 sc1
	v_add_u32_e32 v68, 0x1000, v68
	global_store_dword v68, v64, s[38:39] sc0 sc1
	s_waitcnt vmcnt(0)
	s_barrier
	v_cmp_eq_u32_e32 vcc, 0, v203
	s_and_saveexec_b64 s[40:41], vcc
	s_cbranch_execz .Lkv_st_done
	v_mov_b32_e32 v69, 0
	v_mov_b32_e32 v70, s32
	global_store_dword v69, v70, s[36:37] sc0 sc1
	s_waitcnt vmcnt(0)
.Lkv_st_done:
	s_or_b64 exec, exec, s[40:41]
	s_branch .LBB0_583
.Lkv_merge:
	v_cmp_eq_u32_e32 vcc, 0, v203
	s_and_saveexec_b64 s[40:41], vcc
	s_cbranch_execz .Lkv_pdone
	v_mov_b32_e32 v69, 0
	s_mov_b32 s30, 0
.Lkv_poll:
	global_load_dword v70, v69, s[36:37] sc0 sc1
	s_waitcnt vmcnt(0)
	v_cmp_eq_u32_e32 vcc, s32, v70
	s_nop 4
	s_cbranch_vccnz .Lkv_got
	s_sleep 8
	s_add_i32 s30, s30, 1
	s_cmp_lt_u32 s30, 0x400000
	s_cbranch_scc1 .Lkv_poll
.Lkv_got:
.Lkv_pdone:
	s_or_b64 exec, exec, s[40:41]
	s_barrier
	global_load_dword v100, v68, s[38:39] sc0 sc1
	global_load_dword v101, v68, s[38:39] offset:256 sc0 sc1
	global_load_dword v102, v68, s[38:39] offset:512 sc0 sc1
	global_load_dword v103, v68, s[38:39] offset:768 sc0 sc1
	global_load_dword v104, v68, s[38:39] offset:1024 sc0 sc1
	global_load_dword v105, v68, s[38:39] offset:1280 sc0 sc1
	global_load_dword v106, v68, s[38:39] offset:1536 sc0 sc1
	global_load_dword v107, v68, s[38:39] offset:1792 sc0 sc1
	global_load_dword v108, v68, s[38:39] offset:2048 sc0 sc1
	global_load_dword v109, v68, s[38:39] offset:2304 sc0 sc1
	global_load_dword v110, v68, s[38:39] offset:2560 sc0 sc1
	global_load_dword v111, v68, s[38:39] offset:2816 sc0 sc1
	global_load_dword v112, v68, s[38:39] offset:3072 sc0 sc1
	global_load_dword v113, v68, s[38:39] offset:3328 sc0 sc1
	global_load_dword v114, v68, s[38:39] offset:3584 sc0 sc1
	global_load_dword v115, v68, s[38:39] offset:3840 sc0 sc1
	v_add_u32_e32 v68, 0x1000, v68
	s_waitcnt vmcnt(0)
	v_add_f32_e32 v0, v0, v100
	v_add_f32_e32 v1, v1, v101
	v_add_f32_e32 v2, v2, v102
	v_add_f32_e32 v3, v3, v103
	v_add_f32_e32 v4, v4, v104
	v_add_f32_e32 v5, v5, v105
	v_add_f32_e32 v6, v6, v106
	v_add_f32_e32 v7, v7, v107
	v_add_f32_e32 v8, v8, v108
	v_add_f32_e32 v9, v9, v109
	v_add_f32_e32 v10, v10, v110
	v_add_f32_e32 v11, v11, v111
	v_add_f32_e32 v12, v12, v112
	v_add_f32_e32 v13, v13, v113
	v_add_f32_e32 v14, v14, v114
	v_add_f32_e32 v15, v15, v115
	global_load_dword v100, v68, s[38:39] sc0 sc1
	global_load_dword v101, v68, s[38:39] offset:256 sc0 sc1
	global_load_dword v102, v68, s[38:39] offset:512 sc0 sc1
	global_load_dword v103, v68, s[38:39] offset:768 sc0 sc1
	global_load_dword v104, v68, s[38:39] offset:1024 sc0 sc1
	global_load_dword v105, v68, s[38:39] offset:1280 sc0 sc1
	global_load_dword v106, v68, s[38:39] offset:1536 sc0 sc1
	global_load_dword v107, v68, s[38:39] offset:1792 sc0 sc1
	global_load_dword v108, v68, s[38:39] offset:2048 sc0 sc1
	global_load_dword v109, v68, s[38:39] offset:2304 sc0 sc1
	global_load_dword v110, v68, s[38:39] offset:2560 sc0 sc1
	global_load_dword v111, v68, s[38:39] offset:2816 sc0 sc1
	global_load_dword v112, v68, s[38:39] offset:3072 sc0 sc1
	global_load_dword v113, v68, s[38:39] offset:3328 sc0 sc1
	global_load_dword v114, v68, s[38:39] offset:3584 sc0 sc1
	global_load_dword v115, v68, s[38:39] offset:3840 sc0 sc1
	v_add_u32_e32 v68, 0x1000, v68
	s_waitcnt vmcnt(0)
	v_add_f32_e32 v16, v16, v100
	v_add_f32_e32 v17, v17, v101
	v_add_f32_e32 v18, v18, v102
	v_add_f32_e32 v19, v19, v103
	v_add_f32_e32 v20, v20, v104
	v_add_f32_e32 v21, v21, v105
	v_add_f32_e32 v22, v22, v106
	v_add_f32_e32 v23, v23, v107
	v_add_f32_e32 v24, v24, v108
	v_add_f32_e32 v25, v25, v109
	v_add_f32_e32 v26, v26, v110
	v_add_f32_e32 v27, v27, v111
	v_add_f32_e32 v28, v28, v112
	v_add_f32_e32 v29, v29, v113
	v_add_f32_e32 v30, v30, v114
	v_add_f32_e32 v31, v31, v115
	global_load_dword v100, v68, s[38:39] sc0 sc1
	global_load_dword v101, v68, s[38:39] offset:256 sc0 sc1
	global_load_dword v102, v68, s[38:39] offset:512 sc0 sc1
	global_load_dword v103, v68, s[38:39] offset:768 sc0 sc1
	global_load_dword v104, v68, s[38:39] offset:1024 sc0 sc1
	global_load_dword v105, v68, s[38:39] offset:1280 sc0 sc1
	global_load_dword v106, v68, s[38:39] offset:1536 sc0 sc1
	global_load_dword v107, v68, s[38:39] offset:1792 sc0 sc1
	global_load_dword v108, v68, s[38:39] offset:2048 sc0 sc1
	global_load_dword v109, v68, s[38:39] offset:2304 sc0 sc1
	global_load_dword v110, v68, s[38:39] offset:2560 sc0 sc1
	global_load_dword v111, v68, s[38:39] offset:2816 sc0 sc1
	global_load_dword v112, v68, s[38:39] offset:3072 sc0 sc1
	global_load_dword v113, v68, s[38:39] offset:3328 sc0 sc1
	global_load_dword v114, v68, s[38:39] offset:3584 sc0 sc1
	global_load_dword v115, v68, s[38:39] offset:3840 sc0 sc1
	v_add_u32_e32 v68, 0x1000, v68
	s_waitcnt vmcnt(0)
	v_add_f32_e32 v32, v32, v100
	v_add_f32_e32 v33, v33, v101
	v_add_f32_e32 v34, v34, v102
	v_add_f32_e32 v35, v35, v103
	v_add_f32_e32 v36, v36, v104
	v_add_f32_e32 v37, v37, v105
	v_add_f32_e32 v38, v38, v106
	v_add_f32_e32 v39, v39, v107
	v_add_f32_e32 v40, v40, v108
	v_add_f32_e32 v41, v41, v109
	v_add_f32_e32 v42, v42, v110
	v_add_f32_e32 v43, v43, v111
	v_add_f32_e32 v44, v44, v112
	v_add_f32_e32 v45, v45, v113
	v_add_f32_e32 v46, v46, v114
	v_add_f32_e32 v47, v47, v115
	global_load_dword v100, v68, s[38:39] sc0 sc1
	global_load_dword v101, v68, s[38:39] offset:256 sc0 sc1
	global_load_dword v102, v68, s[38:39] offset:512 sc0 sc1
	global_load_dword v103, v68, s[38:39] offset:768 sc0 sc1
	global_load_dword v104, v68, s[38:39] offset:1024 sc0 sc1
	global_load_dword v105, v68, s[38:39] offset:1280 sc0 sc1
	global_load_dword v106, v68, s[38:39] offset:1536 sc0 sc1
	global_load_dword v107, v68, s[38:39] offset:1792 sc0 sc1
	global_load_dword v108, v68, s[38:39] offset:2048 sc0 sc1
	global_load_dword v109, v68, s[38:39] offset:2304 sc0 sc1
	global_load_dword v110, v68, s[38:39] offset:2560 sc0 sc1
	global_load_dword v111, v68, s[38:39] offset:2816 sc0 sc1
	global_load_dword v112, v68, s[38:39] offset:3072 sc0 sc1
	global_load_dword v113, v68, s[38:39] offset:3328 sc0 sc1
	global_load_dword v114, v68, s[38:39] offset:3584 sc0 sc1
	global_load_dword v115, v68, s[38:39] offset:3840 sc0 sc1
	v_add_u32_e32 v68, 0x1000, v68
	global_load_dword v116, v68, s[38:39] sc0 sc1
	s_waitcnt vmcnt(0)
	v_add_f32_e32 v48, v48, v100
	v_add_f32_e32 v49, v49, v101
	v_add_f32_e32 v50, v50, v102
	v_add_f32_e32 v51, v51, v103
	v_add_f32_e32 v52, v52, v104
	v_add_f32_e32 v53, v53, v105
	v_add_f32_e32 v54, v54, v106
	v_add_f32_e32 v55, v55, v107
	v_add_f32_e32 v56, v56, v108
	v_add_f32_e32 v57, v57, v109
	v_add_f32_e32 v58, v58, v110
	v_add_f32_e32 v59, v59, v111
	v_add_f32_e32 v60, v60, v112
	v_add_f32_e32 v61, v61, v113
	v_add_f32_e32 v62, v62, v114
	v_add_f32_e32 v63, v63, v115
	v_add_f32_e32 v183, v64, v116
	v_mov_b32_e32 v64, 0
	v_mov_b32_e32 v65, 0
	v_mov_b32_e32 v66, 0
	v_mov_b32_e32 v67, 0
	v_cmp_gt_u32_e32 vcc, 32, v202
	s_nop 1
	s_branch .Lkv_resume

.LBB0_1026:
	v_ashrrev_i32_e32 v13, 31, v12
	v_lshl_add_u64 v[0:1], v[12:13], 2, s[4:5]
	v_lshl_add_u64 v[2:3], v[0:1], 0, v[192:193]
	global_load_dwordx4 v[4:7], v[2:3], off offset:32
	global_load_dwordx4 v[8:11], v[2:3], off offset:16
	global_load_dwordx4 v[68:71], v[2:3], off
	s_mov_b64 s[0:1], 0x300000
	v_lshl_add_u64 v[158:159], v[2:3], 0, s[0:1]
	s_mov_b32 s0, 0x300000
	v_mov_b32_e32 v15, v193
	v_mov_b32_e32 v17, v193
	v_mov_b32_e32 v19, v193
	v_mov_b32_e32 v21, v193
	v_mov_b32_e32 v23, v193
	v_mov_b32_e32 v25, v193
	v_mov_b32_e32 v27, v193
	v_mov_b32_e32 v29, v193
	v_mov_b32_e32 v31, v193
	v_mov_b32_e32 v33, v193
	v_mov_b32_e32 v35, v193
	v_mov_b32_e32 v37, v193
	v_mov_b32_e32 v39, v193
	v_mov_b32_e32 v41, v193
	v_mov_b32_e32 v43, v193
	v_mov_b32_e32 v45, v193
	v_mov_b32_e32 v47, v193
	v_mov_b32_e32 v49, v193
	v_mov_b32_e32 v51, v193
	v_mov_b32_e32 v53, v193
	v_mov_b32_e32 v55, v193
	v_mov_b32_e32 v57, v193
	v_mov_b32_e32 v59, v193
	v_mov_b32_e32 v61, v193
	v_mov_b32_e32 v63, v193
	v_mov_b32_e32 v65, v193
	v_mov_b32_e32 v67, v193
	s_waitcnt vmcnt(2)
	v_fma_f32 v140, v73, v4, 0
	v_fma_f32 v139, v74, v4, 0
	v_add_co_u32_e64 v4, s[0:1], s0, v2
	v_fma_f32 v138, v73, v5, 0
	v_fma_f32 v137, v74, v5, 0
	v_addc_co_u32_e64 v5, s[0:1], 0, v3, s[0:1]
	s_waitcnt vmcnt(0)
	v_fma_f32 v156, v73, v68, 0
	v_fma_f32 v155, v74, v68, 0
	v_fma_f32 v154, v73, v69, 0
	v_fma_f32 v153, v74, v69, 0
	v_fma_f32 v152, v73, v70, 0
	v_fma_f32 v151, v74, v70, 0
	v_fma_f32 v150, v73, v71, 0
	v_fma_f32 v149, v74, v71, 0
	v_fma_f32 v148, v73, v8, 0
	v_fma_f32 v147, v74, v8, 0
	v_fma_f32 v146, v73, v9, 0
	v_fma_f32 v145, v74, v9, 0
	v_fma_f32 v144, v73, v10, 0
	v_fma_f32 v143, v74, v10, 0
	v_fma_f32 v142, v73, v11, 0
	v_fma_f32 v141, v74, v11, 0
	v_fma_f32 v71, v73, v6, 0
	v_fma_f32 v70, v74, v6, 0
	v_fma_f32 v69, v73, v7, 0
	v_fma_f32 v68, v74, v7, 0
	global_load_dwordx4 v[4:7], v[4:5], off
	s_nop 0
	global_load_dwordx4 v[8:11], v[158:159], off offset:32
	s_nop 0
	global_load_dwordx4 v[158:161], v[158:159], off offset:16
	s_mov_b64 s[0:1], 0x600000
	s_waitcnt vmcnt(2)
	v_fmac_f32_e32 v156, v75, v4
	v_fmac_f32_e32 v155, v76, v4
	s_waitcnt vmcnt(0)
	v_fmac_f32_e32 v148, v75, v158
	v_fmac_f32_e32 v147, v76, v158
	v_fmac_f32_e32 v146, v75, v159
	v_fmac_f32_e32 v145, v76, v159
	v_lshl_add_u64 v[158:159], v[2:3], 0, s[0:1]
	s_mov_b32 s0, 0x600000
	v_add_co_u32_e64 v4, s[0:1], s0, v2
	v_fmac_f32_e32 v154, v75, v5
	v_fmac_f32_e32 v153, v76, v5
	v_addc_co_u32_e64 v5, s[0:1], 0, v3, s[0:1]
	v_fmac_f32_e32 v152, v75, v6
	v_fmac_f32_e32 v151, v76, v6
	v_fmac_f32_e32 v150, v75, v7
	v_fmac_f32_e32 v149, v76, v7
	v_fmac_f32_e32 v144, v75, v160
	v_fmac_f32_e32 v143, v76, v160
	v_fmac_f32_e32 v142, v75, v161
	v_fmac_f32_e32 v141, v76, v161
	v_fmac_f32_e32 v140, v75, v8
	v_fmac_f32_e32 v139, v76, v8
	v_fmac_f32_e32 v138, v75, v9
	v_fmac_f32_e32 v137, v76, v9
	v_fmac_f32_e32 v71, v75, v10
	v_fmac_f32_e32 v70, v76, v10
	v_fmac_f32_e32 v69, v75, v11
	v_fmac_f32_e32 v68, v76, v11
	global_load_dwordx4 v[4:7], v[4:5], off
	s_nop 0
	global_load_dwordx4 v[8:11], v[158:159], off offset:32
	s_nop 0
	global_load_dwordx4 v[158:161], v[158:159], off offset:16
	s_mov_b64 s[0:1], 0x900000
	s_waitcnt vmcnt(2)
	v_fmac_f32_e32 v156, v77, v4
	v_fmac_f32_e32 v155, v78, v4
	s_waitcnt vmcnt(0)
	v_fmac_f32_e32 v148, v77, v158
	v_fmac_f32_e32 v147, v78, v158
	v_fmac_f32_e32 v146, v77, v159
	v_fmac_f32_e32 v145, v78, v159
	v_lshl_add_u64 v[158:159], v[2:3], 0, s[0:1]
	s_mov_b32 s0, 0x900000
	v_add_co_u32_e64 v4, s[0:1], s0, v2
	v_fmac_f32_e32 v154, v77, v5
	v_fmac_f32_e32 v153, v78, v5
	v_addc_co_u32_e64 v5, s[0:1], 0, v3, s[0:1]
	v_fmac_f32_e32 v152, v77, v6
	v_fmac_f32_e32 v151, v78, v6
	v_fmac_f32_e32 v150, v77, v7
	v_fmac_f32_e32 v149, v78, v7
	v_fmac_f32_e32 v144, v77, v160
	v_fmac_f32_e32 v143, v78, v160
	v_fmac_f32_e32 v142, v77, v161
	v_fmac_f32_e32 v141, v78, v161
	v_fmac_f32_e32 v140, v77, v8
	v_fmac_f32_e32 v139, v78, v8
	v_fmac_f32_e32 v138, v77, v9
	v_fmac_f32_e32 v137, v78, v9
	v_fmac_f32_e32 v71, v77, v10
	v_fmac_f32_e32 v70, v78, v10
	v_fmac_f32_e32 v69, v77, v11
	v_fmac_f32_e32 v68, v78, v11
	global_load_dwordx4 v[4:7], v[4:5], off
	s_nop 0
	global_load_dwordx4 v[8:11], v[158:159], off offset:32
	s_nop 0
	global_load_dwordx4 v[158:161], v[158:159], off offset:16
	s_mov_b64 s[0:1], 0xc00000
	s_waitcnt vmcnt(2)
	v_fmac_f32_e32 v156, v79, v4
	s_waitcnt vmcnt(1)
	v_fmac_f32_e32 v71, v79, v10
	v_fmac_f32_e32 v70, v80, v10
	v_fmac_f32_e32 v69, v79, v11
	v_fmac_f32_e32 v68, v80, v11
	v_lshl_add_u64 v[10:11], v[2:3], 0, s[0:1]
	s_mov_b32 s0, 0xc00000
	v_add_co_u32_e64 v2, s[0:1], s0, v2
	v_fmac_f32_e32 v155, v80, v4
	s_nop 0
	v_addc_co_u32_e64 v3, s[0:1], 0, v3, s[0:1]
	v_fmac_f32_e32 v154, v79, v5
	v_fmac_f32_e32 v153, v80, v5
	v_fmac_f32_e32 v152, v79, v6
	v_fmac_f32_e32 v151, v80, v6
	v_fmac_f32_e32 v150, v79, v7
	v_fmac_f32_e32 v149, v80, v7
	s_waitcnt vmcnt(0)
	v_fmac_f32_e32 v148, v79, v158
	v_fmac_f32_e32 v147, v80, v158
	v_fmac_f32_e32 v146, v79, v159
	v_fmac_f32_e32 v145, v80, v159
	v_fmac_f32_e32 v144, v79, v160
	v_fmac_f32_e32 v143, v80, v160
	v_fmac_f32_e32 v142, v79, v161
	v_fmac_f32_e32 v141, v80, v161
	v_fmac_f32_e32 v140, v79, v8
	v_fmac_f32_e32 v139, v80, v8
	v_fmac_f32_e32 v138, v79, v9
	v_fmac_f32_e32 v137, v80, v9
	global_load_dwordx4 v[2:5], v[2:3], off
	s_nop 0
	global_load_dwordx4 v[6:9], v[10:11], off offset:32
	global_load_dwordx4 v[158:161], v[10:11], off offset:16
	v_lshl_add_u64 v[10:11], v[0:1], 0, v[14:15]
	s_waitcnt vmcnt(2)
	v_fmac_f32_e32 v156, v81, v2
	v_fmac_f32_e32 v155, v82, v2
	v_fmac_f32_e32 v154, v81, v3
	v_fmac_f32_e32 v153, v82, v3
	v_fmac_f32_e32 v152, v81, v4
	v_fmac_f32_e32 v151, v82, v4
	v_fmac_f32_e32 v150, v81, v5
	v_fmac_f32_e32 v149, v82, v5
	s_waitcnt vmcnt(0)
	v_fmac_f32_e32 v148, v81, v158
	v_fmac_f32_e32 v147, v82, v158
	v_fmac_f32_e32 v146, v81, v159
	v_fmac_f32_e32 v145, v82, v159
	v_fmac_f32_e32 v144, v81, v160
	v_fmac_f32_e32 v143, v82, v160
	v_fmac_f32_e32 v142, v81, v161
	v_fmac_f32_e32 v141, v82, v161
	v_fmac_f32_e32 v140, v81, v6
	v_fmac_f32_e32 v139, v82, v6
	v_fmac_f32_e32 v138, v81, v7
	v_fmac_f32_e32 v137, v82, v7
	v_fmac_f32_e32 v71, v81, v8
	v_fmac_f32_e32 v70, v82, v8
	v_fmac_f32_e32 v69, v81, v9
	v_fmac_f32_e32 v68, v82, v9
	global_load_dwordx4 v[2:5], v[10:11], off offset:32
	global_load_dwordx4 v[6:9], v[10:11], off offset:16
	global_load_dwordx4 v[158:161], v[10:11], off
	v_lshl_add_u64 v[10:11], v[0:1], 0, v[16:17]
	global_load_dwordx4 v[164:167], v[10:11], off offset:32
	global_load_dwordx4 v[168:171], v[10:11], off offset:16
	global_load_dwordx4 v[172:175], v[10:11], off
	v_lshl_add_u64 v[10:11], v[0:1], 0, v[18:19]
	global_load_dwordx4 v[176:179], v[10:11], off offset:32
	global_load_dwordx4 v[180:183], v[10:11], off offset:16
	global_load_dwordx4 v[184:187], v[10:11], off
	v_lshl_add_u64 v[10:11], v[0:1], 0, v[20:21]
	global_load_dwordx4 v[200:203], v[10:11], off offset:32
	global_load_dwordx4 v[204:207], v[10:11], off offset:16
	global_load_dwordx4 v[208:211], v[10:11], off
	v_lshl_add_u64 v[10:11], v[0:1], 0, v[22:23]
	global_load_dwordx4 v[218:221], v[10:11], off offset:32
	global_load_dwordx4 v[222:225], v[10:11], off offset:16
	global_load_dwordx4 v[226:229], v[10:11], off
	v_lshl_add_u64 v[10:11], v[0:1], 0, v[24:25]
	global_load_dwordx4 v[230:233], v[10:11], off offset:32
	global_load_dwordx4 v[234:237], v[10:11], off offset:16
	global_load_dwordx4 v[238:241], v[10:11], off
	v_lshl_add_u64 v[10:11], v[0:1], 0, v[26:27]
	global_load_dwordx4 v[242:245], v[10:11], off offset:32
	global_load_dwordx4 v[246:249], v[10:11], off offset:16
	global_load_dwordx4 v[250:253], v[10:11], off
	s_waitcnt vmcnt(20)
	v_fmac_f32_e32 v140, v83, v2
	s_waitcnt vmcnt(19)
	v_fmac_f32_e32 v148, v83, v6
	s_waitcnt vmcnt(18)
	v_fmac_f32_e32 v156, v83, v158
	v_fmac_f32_e32 v155, v84, v158
	v_fmac_f32_e32 v154, v83, v159
	v_fmac_f32_e32 v153, v84, v159
	v_fmac_f32_e32 v152, v83, v160
	v_fmac_f32_e32 v151, v84, v160
	v_fmac_f32_e32 v150, v83, v161
	v_fmac_f32_e32 v149, v84, v161
	v_fmac_f32_e32 v147, v84, v6
	v_fmac_f32_e32 v146, v83, v7
	v_fmac_f32_e32 v145, v84, v7
	v_fmac_f32_e32 v144, v83, v8
	v_fmac_f32_e32 v143, v84, v8
	v_fmac_f32_e32 v142, v83, v9
	v_fmac_f32_e32 v141, v84, v9
	v_fmac_f32_e32 v139, v84, v2
	v_fmac_f32_e32 v138, v83, v3
	v_fmac_f32_e32 v137, v84, v3
	v_fmac_f32_e32 v71, v83, v4
	v_fmac_f32_e32 v70, v84, v4
	v_fmac_f32_e32 v69, v83, v5
	v_fmac_f32_e32 v68, v84, v5
	v_lshl_add_u64 v[10:11], v[0:1], 0, v[28:29]
	global_load_dwordx4 v[2:5], v[10:11], off offset:32
	global_load_dwordx4 v[6:9], v[10:11], off offset:16
	global_load_dwordx4 v[158:161], v[10:11], off
	s_waitcnt vmcnt(20)
	v_fmac_f32_e32 v140, v85, v164
	s_waitcnt vmcnt(19)
	v_fmac_f32_e32 v148, v85, v168
	s_waitcnt vmcnt(18)
	v_fmac_f32_e32 v156, v85, v172
	v_fmac_f32_e32 v155, v86, v172
	v_fmac_f32_e32 v154, v85, v173
	v_fmac_f32_e32 v153, v86, v173
	v_fmac_f32_e32 v152, v85, v174
	v_fmac_f32_e32 v151, v86, v174
	v_fmac_f32_e32 v150, v85, v175
	v_fmac_f32_e32 v149, v86, v175
	v_fmac_f32_e32 v147, v86, v168
	v_fmac_f32_e32 v146, v85, v169
	v_fmac_f32_e32 v145, v86, v169
	v_fmac_f32_e32 v144, v85, v170
	v_fmac_f32_e32 v143, v86, v170
	v_fmac_f32_e32 v142, v85, v171
	v_fmac_f32_e32 v141, v86, v171
	v_fmac_f32_e32 v139, v86, v164
	v_fmac_f32_e32 v138, v85, v165
	v_fmac_f32_e32 v137, v86, v165
	v_fmac_f32_e32 v71, v85, v166
	v_fmac_f32_e32 v70, v86, v166
	v_fmac_f32_e32 v69, v85, v167
	v_fmac_f32_e32 v68, v86, v167
	v_lshl_add_u64 v[10:11], v[0:1], 0, v[30:31]
	global_load_dwordx4 v[164:167], v[10:11], off offset:32
	global_load_dwordx4 v[168:171], v[10:11], off offset:16
	global_load_dwordx4 v[172:175], v[10:11], off
	s_waitcnt vmcnt(20)
	v_fmac_f32_e32 v140, v87, v176
	s_waitcnt vmcnt(19)
	v_fmac_f32_e32 v148, v87, v180
	s_waitcnt vmcnt(18)
	v_fmac_f32_e32 v156, v87, v184
	v_fmac_f32_e32 v155, v88, v184
	v_fmac_f32_e32 v154, v87, v185
	v_fmac_f32_e32 v153, v88, v185
	v_fmac_f32_e32 v152, v87, v186
	v_fmac_f32_e32 v151, v88, v186
	v_fmac_f32_e32 v150, v87, v187
	v_fmac_f32_e32 v149, v88, v187
	v_fmac_f32_e32 v147, v88, v180
	v_fmac_f32_e32 v146, v87, v181
	v_fmac_f32_e32 v145, v88, v181
	v_fmac_f32_e32 v144, v87, v182
	v_fmac_f32_e32 v143, v88, v182
	v_fmac_f32_e32 v142, v87, v183
	v_fmac_f32_e32 v141, v88, v183
	v_fmac_f32_e32 v139, v88, v176
	v_fmac_f32_e32 v138, v87, v177
	v_fmac_f32_e32 v137, v88, v177
	v_fmac_f32_e32 v71, v87, v178
	v_fmac_f32_e32 v70, v88, v178
	v_fmac_f32_e32 v69, v87, v179
	v_fmac_f32_e32 v68, v88, v179
	v_lshl_add_u64 v[10:11], v[0:1], 0, v[32:33]
	global_load_dwordx4 v[176:179], v[10:11], off offset:32
	global_load_dwordx4 v[180:183], v[10:11], off offset:16
	global_load_dwordx4 v[184:187], v[10:11], off
	s_waitcnt vmcnt(20)
	v_fmac_f32_e32 v140, v89, v200
	s_waitcnt vmcnt(19)
	v_fmac_f32_e32 v148, v89, v204
	s_waitcnt vmcnt(18)
	v_fmac_f32_e32 v156, v89, v208
	v_fmac_f32_e32 v155, v90, v208
	v_fmac_f32_e32 v154, v89, v209
	v_fmac_f32_e32 v153, v90, v209
	v_fmac_f32_e32 v152, v89, v210
	v_fmac_f32_e32 v151, v90, v210
	v_fmac_f32_e32 v150, v89, v211
	v_fmac_f32_e32 v149, v90, v211
	v_fmac_f32_e32 v147, v90, v204
	v_fmac_f32_e32 v146, v89, v205
	v_fmac_f32_e32 v145, v90, v205
	v_fmac_f32_e32 v144, v89, v206
	v_fmac_f32_e32 v143, v90, v206
	v_fmac_f32_e32 v142, v89, v207
	v_fmac_f32_e32 v141, v90, v207
	v_fmac_f32_e32 v139, v90, v200
	v_fmac_f32_e32 v138, v89, v201
	v_fmac_f32_e32 v137, v90, v201
	v_fmac_f32_e32 v71, v89, v202
	v_fmac_f32_e32 v70, v90, v202
	v_fmac_f32_e32 v69, v89, v203
	v_fmac_f32_e32 v68, v90, v203
	v_lshl_add_u64 v[10:11], v[0:1], 0, v[34:35]
	global_load_dwordx4 v[200:203], v[10:11], off offset:32
	global_load_dwordx4 v[204:207], v[10:11], off offset:16
	global_load_dwordx4 v[208:211], v[10:11], off
	s_waitcnt vmcnt(20)
	v_fmac_f32_e32 v140, v91, v218
	s_waitcnt vmcnt(19)
	v_fmac_f32_e32 v148, v91, v222
	s_waitcnt vmcnt(18)
	v_fmac_f32_e32 v156, v91, v226
	v_fmac_f32_e32 v155, v92, v226
	v_fmac_f32_e32 v154, v91, v227
	v_fmac_f32_e32 v153, v92, v227
	v_fmac_f32_e32 v152, v91, v228
	v_fmac_f32_e32 v151, v92, v228
	v_fmac_f32_e32 v150, v91, v229
	v_fmac_f32_e32 v149, v92, v229
	v_fmac_f32_e32 v147, v92, v222
	v_fmac_f32_e32 v146, v91, v223
	v_fmac_f32_e32 v145, v92, v223
	v_fmac_f32_e32 v144, v91, v224
	v_fmac_f32_e32 v143, v92, v224
	v_fmac_f32_e32 v142, v91, v225
	v_fmac_f32_e32 v141, v92, v225
	v_fmac_f32_e32 v139, v92, v218
	v_fmac_f32_e32 v138, v91, v219
	v_fmac_f32_e32 v137, v92, v219
	v_fmac_f32_e32 v71, v91, v220
	v_fmac_f32_e32 v70, v92, v220
	v_fmac_f32_e32 v69, v91, v221
	v_fmac_f32_e32 v68, v92, v221
	v_lshl_add_u64 v[10:11], v[0:1], 0, v[36:37]
	global_load_dwordx4 v[218:221], v[10:11], off offset:32
	global_load_dwordx4 v[222:225], v[10:11], off offset:16
	global_load_dwordx4 v[226:229], v[10:11], off
	s_waitcnt vmcnt(20)
	v_fmac_f32_e32 v140, v93, v230
	s_waitcnt vmcnt(19)
	v_fmac_f32_e32 v148, v93, v234
	s_waitcnt vmcnt(18)
	v_fmac_f32_e32 v156, v93, v238
	v_fmac_f32_e32 v155, v94, v238
	v_fmac_f32_e32 v154, v93, v239
	v_fmac_f32_e32 v153, v94, v239
	v_fmac_f32_e32 v152, v93, v240
	v_fmac_f32_e32 v151, v94, v240
	v_fmac_f32_e32 v150, v93, v241
	v_fmac_f32_e32 v149, v94, v241
	v_fmac_f32_e32 v147, v94, v234
	v_fmac_f32_e32 v146, v93, v235
	v_fmac_f32_e32 v145, v94, v235
	v_fmac_f32_e32 v144, v93, v236
	v_fmac_f32_e32 v143, v94, v236
	v_fmac_f32_e32 v142, v93, v237
	v_fmac_f32_e32 v141, v94, v237
	v_fmac_f32_e32 v139, v94, v230
	v_fmac_f32_e32 v138, v93, v231
	v_fmac_f32_e32 v137, v94, v231
	v_fmac_f32_e32 v71, v93, v232
	v_fmac_f32_e32 v70, v94, v232
	v_fmac_f32_e32 v69, v93, v233
	v_fmac_f32_e32 v68, v94, v233
	v_lshl_add_u64 v[10:11], v[0:1], 0, v[38:39]
	global_load_dwordx4 v[230:233], v[10:11], off offset:32
	global_load_dwordx4 v[234:237], v[10:11], off offset:16
	global_load_dwordx4 v[238:241], v[10:11], off
	s_waitcnt vmcnt(20)
	v_fmac_f32_e32 v140, v95, v242
	s_waitcnt vmcnt(19)
	v_fmac_f32_e32 v148, v95, v246
	s_waitcnt vmcnt(18)
	v_fmac_f32_e32 v156, v95, v250
	v_fmac_f32_e32 v155, v96, v250
	v_fmac_f32_e32 v154, v95, v251
	v_fmac_f32_e32 v153, v96, v251
	v_fmac_f32_e32 v152, v95, v252
	v_fmac_f32_e32 v151, v96, v252
	v_fmac_f32_e32 v150, v95, v253
	v_fmac_f32_e32 v149, v96, v253
	v_fmac_f32_e32 v147, v96, v246
	v_fmac_f32_e32 v146, v95, v247
	v_fmac_f32_e32 v145, v96, v247
	v_fmac_f32_e32 v144, v95, v248
	v_fmac_f32_e32 v143, v96, v248
	v_fmac_f32_e32 v142, v95, v249
	v_fmac_f32_e32 v141, v96, v249
	v_fmac_f32_e32 v139, v96, v242
	v_fmac_f32_e32 v138, v95, v243
	v_fmac_f32_e32 v137, v96, v243
	v_fmac_f32_e32 v71, v95, v244
	v_fmac_f32_e32 v70, v96, v244
	v_fmac_f32_e32 v69, v95, v245
	v_fmac_f32_e32 v68, v96, v245
	v_lshl_add_u64 v[10:11], v[0:1], 0, v[40:41]
	global_load_dwordx4 v[242:245], v[10:11], off offset:32
	global_load_dwordx4 v[246:249], v[10:11], off offset:16
	global_load_dwordx4 v[250:253], v[10:11], off
	s_waitcnt vmcnt(20)
	v_fmac_f32_e32 v140, v97, v2
	s_waitcnt vmcnt(19)
	v_fmac_f32_e32 v148, v97, v6
	s_waitcnt vmcnt(18)
	v_fmac_f32_e32 v156, v97, v158
	v_fmac_f32_e32 v155, v98, v158
	v_fmac_f32_e32 v154, v97, v159
	v_fmac_f32_e32 v153, v98, v159
	v_fmac_f32_e32 v152, v97, v160
	v_fmac_f32_e32 v151, v98, v160
	v_fmac_f32_e32 v150, v97, v161
	v_fmac_f32_e32 v149, v98, v161
	v_fmac_f32_e32 v147, v98, v6
	v_fmac_f32_e32 v146, v97, v7
	v_fmac_f32_e32 v145, v98, v7
	v_fmac_f32_e32 v144, v97, v8
	v_fmac_f32_e32 v143, v98, v8
	v_fmac_f32_e32 v142, v97, v9
	v_fmac_f32_e32 v141, v98, v9
	v_fmac_f32_e32 v139, v98, v2
	v_fmac_f32_e32 v138, v97, v3
	v_fmac_f32_e32 v137, v98, v3
	v_fmac_f32_e32 v71, v97, v4
	v_fmac_f32_e32 v70, v98, v4
	v_fmac_f32_e32 v69, v97, v5
	v_fmac_f32_e32 v68, v98, v5
	v_lshl_add_u64 v[10:11], v[0:1], 0, v[42:43]
	global_load_dwordx4 v[2:5], v[10:11], off offset:32
	global_load_dwordx4 v[6:9], v[10:11], off offset:16
	global_load_dwordx4 v[158:161], v[10:11], off
	s_waitcnt vmcnt(20)
	v_fmac_f32_e32 v140, v99, v164
	s_waitcnt vmcnt(19)
	v_fmac_f32_e32 v148, v99, v168
	s_waitcnt vmcnt(18)
	v_fmac_f32_e32 v156, v99, v172
	v_fmac_f32_e32 v155, v100, v172
	v_fmac_f32_e32 v154, v99, v173
	v_fmac_f32_e32 v153, v100, v173
	v_fmac_f32_e32 v152, v99, v174
	v_fmac_f32_e32 v151, v100, v174
	v_fmac_f32_e32 v150, v99, v175
	v_fmac_f32_e32 v149, v100, v175
	v_fmac_f32_e32 v147, v100, v168
	v_fmac_f32_e32 v146, v99, v169
	v_fmac_f32_e32 v145, v100, v169
	v_fmac_f32_e32 v144, v99, v170
	v_fmac_f32_e32 v143, v100, v170
	v_fmac_f32_e32 v142, v99, v171
	v_fmac_f32_e32 v141, v100, v171
	v_fmac_f32_e32 v139, v100, v164
	v_fmac_f32_e32 v138, v99, v165
	v_fmac_f32_e32 v137, v100, v165
	v_fmac_f32_e32 v71, v99, v166
	v_fmac_f32_e32 v70, v100, v166
	v_fmac_f32_e32 v69, v99, v167
	v_fmac_f32_e32 v68, v100, v167
	v_lshl_add_u64 v[10:11], v[0:1], 0, v[44:45]
	global_load_dwordx4 v[164:167], v[10:11], off offset:32
	global_load_dwordx4 v[168:171], v[10:11], off offset:16
	global_load_dwordx4 v[172:175], v[10:11], off
	s_waitcnt vmcnt(20)
	v_fmac_f32_e32 v140, v101, v176
	s_waitcnt vmcnt(19)
	v_fmac_f32_e32 v148, v101, v180
	s_waitcnt vmcnt(18)
	v_fmac_f32_e32 v156, v101, v184
	v_fmac_f32_e32 v155, v102, v184
	v_fmac_f32_e32 v154, v101, v185
	v_fmac_f32_e32 v153, v102, v185
	v_fmac_f32_e32 v152, v101, v186
	v_fmac_f32_e32 v151, v102, v186
	v_fmac_f32_e32 v150, v101, v187
	v_fmac_f32_e32 v149, v102, v187
	v_fmac_f32_e32 v147, v102, v180
	v_fmac_f32_e32 v146, v101, v181
	v_fmac_f32_e32 v145, v102, v181
	v_fmac_f32_e32 v144, v101, v182
	v_fmac_f32_e32 v143, v102, v182
	v_fmac_f32_e32 v142, v101, v183
	v_fmac_f32_e32 v141, v102, v183
	v_fmac_f32_e32 v139, v102, v176
	v_fmac_f32_e32 v138, v101, v177
	v_fmac_f32_e32 v137, v102, v177
	v_fmac_f32_e32 v71, v101, v178
	v_fmac_f32_e32 v70, v102, v178
	v_fmac_f32_e32 v69, v101, v179
	v_fmac_f32_e32 v68, v102, v179
	v_lshl_add_u64 v[10:11], v[0:1], 0, v[46:47]
	global_load_dwordx4 v[176:179], v[10:11], off offset:32
	global_load_dwordx4 v[180:183], v[10:11], off offset:16
	global_load_dwordx4 v[184:187], v[10:11], off
	s_waitcnt vmcnt(20)
	v_fmac_f32_e32 v140, v103, v200
	s_waitcnt vmcnt(19)
	v_fmac_f32_e32 v148, v103, v204
	s_waitcnt vmcnt(18)
	v_fmac_f32_e32 v156, v103, v208
	v_fmac_f32_e32 v155, v104, v208
	v_fmac_f32_e32 v154, v103, v209
	v_fmac_f32_e32 v153, v104, v209
	v_fmac_f32_e32 v152, v103, v210
	v_fmac_f32_e32 v151, v104, v210
	v_fmac_f32_e32 v150, v103, v211
	v_fmac_f32_e32 v149, v104, v211
	v_fmac_f32_e32 v147, v104, v204
	v_fmac_f32_e32 v146, v103, v205
	v_fmac_f32_e32 v145, v104, v205
	v_fmac_f32_e32 v144, v103, v206
	v_fmac_f32_e32 v143, v104, v206
	v_fmac_f32_e32 v142, v103, v207
	v_fmac_f32_e32 v141, v104, v207
	v_fmac_f32_e32 v139, v104, v200
	v_fmac_f32_e32 v138, v103, v201
	v_fmac_f32_e32 v137, v104, v201
	v_fmac_f32_e32 v71, v103, v202
	v_fmac_f32_e32 v70, v104, v202
	v_fmac_f32_e32 v69, v103, v203
	v_fmac_f32_e32 v68, v104, v203
	v_lshl_add_u64 v[10:11], v[0:1], 0, v[48:49]
	global_load_dwordx4 v[200:203], v[10:11], off offset:32
	global_load_dwordx4 v[204:207], v[10:11], off offset:16
	global_load_dwordx4 v[208:211], v[10:11], off
	s_waitcnt vmcnt(20)
	v_fmac_f32_e32 v140, v105, v218
	s_waitcnt vmcnt(19)
	v_fmac_f32_e32 v148, v105, v222
	s_waitcnt vmcnt(18)
	v_fmac_f32_e32 v156, v105, v226
	v_fmac_f32_e32 v155, v106, v226
	v_fmac_f32_e32 v154, v105, v227
	v_fmac_f32_e32 v153, v106, v227
	v_fmac_f32_e32 v152, v105, v228
	v_fmac_f32_e32 v151, v106, v228
	v_fmac_f32_e32 v150, v105, v229
	v_fmac_f32_e32 v149, v106, v229
	v_fmac_f32_e32 v147, v106, v222
	v_fmac_f32_e32 v146, v105, v223
	v_fmac_f32_e32 v145, v106, v223
	v_fmac_f32_e32 v144, v105, v224
	v_fmac_f32_e32 v143, v106, v224
	v_fmac_f32_e32 v142, v105, v225
	v_fmac_f32_e32 v141, v106, v225
	v_fmac_f32_e32 v139, v106, v218
	v_fmac_f32_e32 v138, v105, v219
	v_fmac_f32_e32 v137, v106, v219
	v_fmac_f32_e32 v71, v105, v220
	v_fmac_f32_e32 v70, v106, v220
	v_fmac_f32_e32 v69, v105, v221
	v_fmac_f32_e32 v68, v106, v221
	v_lshl_add_u64 v[10:11], v[0:1], 0, v[50:51]
	global_load_dwordx4 v[218:221], v[10:11], off offset:32
	global_load_dwordx4 v[222:225], v[10:11], off offset:16
	global_load_dwordx4 v[226:229], v[10:11], off
	s_waitcnt vmcnt(20)
	v_fmac_f32_e32 v140, v107, v230
	s_waitcnt vmcnt(19)
	v_fmac_f32_e32 v148, v107, v234
	s_waitcnt vmcnt(18)
	v_fmac_f32_e32 v156, v107, v238
	v_fmac_f32_e32 v155, v108, v238
	v_fmac_f32_e32 v154, v107, v239
	v_fmac_f32_e32 v153, v108, v239
	v_fmac_f32_e32 v152, v107, v240
	v_fmac_f32_e32 v151, v108, v240
	v_fmac_f32_e32 v150, v107, v241
	v_fmac_f32_e32 v149, v108, v241
	v_fmac_f32_e32 v147, v108, v234
	v_fmac_f32_e32 v146, v107, v235
	v_fmac_f32_e32 v145, v108, v235
	v_fmac_f32_e32 v144, v107, v236
	v_fmac_f32_e32 v143, v108, v236
	v_fmac_f32_e32 v142, v107, v237
	v_fmac_f32_e32 v141, v108, v237
	v_fmac_f32_e32 v139, v108, v230
	v_fmac_f32_e32 v138, v107, v231
	v_fmac_f32_e32 v137, v108, v231
	v_fmac_f32_e32 v71, v107, v232
	v_fmac_f32_e32 v70, v108, v232
	v_fmac_f32_e32 v69, v107, v233
	v_fmac_f32_e32 v68, v108, v233
	v_lshl_add_u64 v[10:11], v[0:1], 0, v[52:53]
	global_load_dwordx4 v[230:233], v[10:11], off offset:32
	global_load_dwordx4 v[234:237], v[10:11], off offset:16
	global_load_dwordx4 v[238:241], v[10:11], off
	s_waitcnt vmcnt(20)
	v_fmac_f32_e32 v140, v109, v242
	s_waitcnt vmcnt(19)
	v_fmac_f32_e32 v148, v109, v246
	s_waitcnt vmcnt(18)
	v_fmac_f32_e32 v156, v109, v250
	v_fmac_f32_e32 v155, v110, v250
	v_fmac_f32_e32 v154, v109, v251
	v_fmac_f32_e32 v153, v110, v251
	v_fmac_f32_e32 v152, v109, v252
	v_fmac_f32_e32 v151, v110, v252
	v_fmac_f32_e32 v150, v109, v253
	v_fmac_f32_e32 v149, v110, v253
	v_fmac_f32_e32 v147, v110, v246
	v_fmac_f32_e32 v146, v109, v247
	v_fmac_f32_e32 v145, v110, v247
	v_fmac_f32_e32 v144, v109, v248
	v_fmac_f32_e32 v143, v110, v248
	v_fmac_f32_e32 v142, v109, v249
	v_fmac_f32_e32 v141, v110, v249
	v_fmac_f32_e32 v139, v110, v242
	v_fmac_f32_e32 v138, v109, v243
	v_fmac_f32_e32 v137, v110, v243
	v_fmac_f32_e32 v71, v109, v244
	v_fmac_f32_e32 v70, v110, v244
	v_fmac_f32_e32 v69, v109, v245
	v_fmac_f32_e32 v68, v110, v245
	v_lshl_add_u64 v[10:11], v[0:1], 0, v[54:55]
	global_load_dwordx4 v[242:245], v[10:11], off offset:32
	global_load_dwordx4 v[246:249], v[10:11], off offset:16
	global_load_dwordx4 v[250:253], v[10:11], off
	s_waitcnt vmcnt(20)
	v_fmac_f32_e32 v140, v111, v2
	s_waitcnt vmcnt(19)
	v_fmac_f32_e32 v148, v111, v6
	s_waitcnt vmcnt(18)
	v_fmac_f32_e32 v156, v111, v158
	v_fmac_f32_e32 v155, v112, v158
	v_fmac_f32_e32 v154, v111, v159
	v_fmac_f32_e32 v153, v112, v159
	v_fmac_f32_e32 v152, v111, v160
	v_fmac_f32_e32 v151, v112, v160
	v_fmac_f32_e32 v150, v111, v161
	v_fmac_f32_e32 v149, v112, v161
	v_fmac_f32_e32 v147, v112, v6
	v_fmac_f32_e32 v146, v111, v7
	v_fmac_f32_e32 v145, v112, v7
	v_fmac_f32_e32 v144, v111, v8
	v_fmac_f32_e32 v143, v112, v8
	v_fmac_f32_e32 v142, v111, v9
	v_fmac_f32_e32 v141, v112, v9
	v_fmac_f32_e32 v139, v112, v2
	v_fmac_f32_e32 v138, v111, v3
	v_fmac_f32_e32 v137, v112, v3
	v_fmac_f32_e32 v71, v111, v4
	v_fmac_f32_e32 v70, v112, v4
	v_fmac_f32_e32 v69, v111, v5
	v_fmac_f32_e32 v68, v112, v5
	v_lshl_add_u64 v[10:11], v[0:1], 0, v[56:57]
	global_load_dwordx4 v[2:5], v[10:11], off offset:32
	global_load_dwordx4 v[6:9], v[10:11], off offset:16
	global_load_dwordx4 v[158:161], v[10:11], off
	s_waitcnt vmcnt(20)
	v_fmac_f32_e32 v140, v113, v164
	s_waitcnt vmcnt(19)
	v_fmac_f32_e32 v148, v113, v168
	s_waitcnt vmcnt(18)
	v_fmac_f32_e32 v156, v113, v172
	v_fmac_f32_e32 v155, v114, v172
	v_fmac_f32_e32 v154, v113, v173
	v_fmac_f32_e32 v153, v114, v173
	v_fmac_f32_e32 v152, v113, v174
	v_fmac_f32_e32 v151, v114, v174
	v_fmac_f32_e32 v150, v113, v175
	v_fmac_f32_e32 v149, v114, v175
	v_fmac_f32_e32 v147, v114, v168
	v_fmac_f32_e32 v146, v113, v169
	v_fmac_f32_e32 v145, v114, v169
	v_fmac_f32_e32 v144, v113, v170
	v_fmac_f32_e32 v143, v114, v170
	v_fmac_f32_e32 v142, v113, v171
	v_fmac_f32_e32 v141, v114, v171
	v_fmac_f32_e32 v139, v114, v164
	v_fmac_f32_e32 v138, v113, v165
	v_fmac_f32_e32 v137, v114, v165
	v_fmac_f32_e32 v71, v113, v166
	v_fmac_f32_e32 v70, v114, v166
	v_fmac_f32_e32 v69, v113, v167
	v_fmac_f32_e32 v68, v114, v167
	v_lshl_add_u64 v[10:11], v[0:1], 0, v[58:59]
	global_load_dwordx4 v[164:167], v[10:11], off offset:32
	global_load_dwordx4 v[168:171], v[10:11], off offset:16
	global_load_dwordx4 v[172:175], v[10:11], off
	s_waitcnt vmcnt(20)
	v_fmac_f32_e32 v140, v115, v176
	s_waitcnt vmcnt(19)
	v_fmac_f32_e32 v148, v115, v180
	s_waitcnt vmcnt(18)
	v_fmac_f32_e32 v156, v115, v184
	v_fmac_f32_e32 v155, v116, v184
	v_fmac_f32_e32 v154, v115, v185
	v_fmac_f32_e32 v153, v116, v185
	v_fmac_f32_e32 v152, v115, v186
	v_fmac_f32_e32 v151, v116, v186
	v_fmac_f32_e32 v150, v115, v187
	v_fmac_f32_e32 v149, v116, v187
	v_fmac_f32_e32 v147, v116, v180
	v_fmac_f32_e32 v146, v115, v181
	v_fmac_f32_e32 v145, v116, v181
	v_fmac_f32_e32 v144, v115, v182
	v_fmac_f32_e32 v143, v116, v182
	v_fmac_f32_e32 v142, v115, v183
	v_fmac_f32_e32 v141, v116, v183
	v_fmac_f32_e32 v139, v116, v176
	v_fmac_f32_e32 v138, v115, v177
	v_fmac_f32_e32 v137, v116, v177
	v_fmac_f32_e32 v71, v115, v178
	v_fmac_f32_e32 v70, v116, v178
	v_fmac_f32_e32 v69, v115, v179
	v_fmac_f32_e32 v68, v116, v179
	v_lshl_add_u64 v[10:11], v[0:1], 0, v[60:61]
	global_load_dwordx4 v[176:179], v[10:11], off offset:32
	global_load_dwordx4 v[180:183], v[10:11], off offset:16
	global_load_dwordx4 v[184:187], v[10:11], off
	s_waitcnt vmcnt(20)
	v_fmac_f32_e32 v140, v117, v200
	s_waitcnt vmcnt(19)
	v_fmac_f32_e32 v148, v117, v204
	s_waitcnt vmcnt(18)
	v_fmac_f32_e32 v156, v117, v208
	v_fmac_f32_e32 v155, v118, v208
	v_fmac_f32_e32 v154, v117, v209
	v_fmac_f32_e32 v153, v118, v209
	v_fmac_f32_e32 v152, v117, v210
	v_fmac_f32_e32 v151, v118, v210
	v_fmac_f32_e32 v150, v117, v211
	v_fmac_f32_e32 v149, v118, v211
	v_fmac_f32_e32 v147, v118, v204
	v_fmac_f32_e32 v146, v117, v205
	v_fmac_f32_e32 v145, v118, v205
	v_fmac_f32_e32 v144, v117, v206
	v_fmac_f32_e32 v143, v118, v206
	v_fmac_f32_e32 v142, v117, v207
	v_fmac_f32_e32 v141, v118, v207
	v_fmac_f32_e32 v139, v118, v200
	v_fmac_f32_e32 v138, v117, v201
	v_fmac_f32_e32 v137, v118, v201
	v_fmac_f32_e32 v71, v117, v202
	v_fmac_f32_e32 v70, v118, v202
	v_fmac_f32_e32 v69, v117, v203
	v_fmac_f32_e32 v68, v118, v203
	v_lshl_add_u64 v[10:11], v[0:1], 0, v[62:63]
	global_load_dwordx4 v[200:203], v[10:11], off offset:32
	global_load_dwordx4 v[204:207], v[10:11], off offset:16
	global_load_dwordx4 v[208:211], v[10:11], off
	s_waitcnt vmcnt(20)
	v_fmac_f32_e32 v140, v119, v218
	s_waitcnt vmcnt(19)
	v_fmac_f32_e32 v148, v119, v222
	s_waitcnt vmcnt(18)
	v_fmac_f32_e32 v156, v119, v226
	v_fmac_f32_e32 v155, v120, v226
	v_fmac_f32_e32 v154, v119, v227
	v_fmac_f32_e32 v153, v120, v227
	v_fmac_f32_e32 v152, v119, v228
	v_fmac_f32_e32 v151, v120, v228
	v_fmac_f32_e32 v150, v119, v229
	v_fmac_f32_e32 v149, v120, v229
	v_fmac_f32_e32 v147, v120, v222
	v_fmac_f32_e32 v146, v119, v223
	v_fmac_f32_e32 v145, v120, v223
	v_fmac_f32_e32 v144, v119, v224
	v_fmac_f32_e32 v143, v120, v224
	v_fmac_f32_e32 v142, v119, v225
	v_fmac_f32_e32 v141, v120, v225
	v_fmac_f32_e32 v139, v120, v218
	v_fmac_f32_e32 v138, v119, v219
	v_fmac_f32_e32 v137, v120, v219
	v_fmac_f32_e32 v71, v119, v220
	v_fmac_f32_e32 v70, v120, v220
	v_fmac_f32_e32 v69, v119, v221
	v_fmac_f32_e32 v68, v120, v221
	s_waitcnt vmcnt(17)
	v_fmac_f32_e32 v140, v121, v230
	s_waitcnt vmcnt(16)
	v_fmac_f32_e32 v148, v121, v234
	s_waitcnt vmcnt(15)
	v_fmac_f32_e32 v156, v121, v238
	v_fmac_f32_e32 v155, v122, v238
	v_fmac_f32_e32 v154, v121, v239
	v_fmac_f32_e32 v153, v122, v239
	v_fmac_f32_e32 v152, v121, v240
	v_fmac_f32_e32 v151, v122, v240
	v_fmac_f32_e32 v150, v121, v241
	v_fmac_f32_e32 v149, v122, v241
	v_fmac_f32_e32 v147, v122, v234
	v_fmac_f32_e32 v146, v121, v235
	v_fmac_f32_e32 v145, v122, v235
	v_fmac_f32_e32 v144, v121, v236
	v_fmac_f32_e32 v143, v122, v236
	v_fmac_f32_e32 v142, v121, v237
	v_fmac_f32_e32 v141, v122, v237
	v_fmac_f32_e32 v139, v122, v230
	v_fmac_f32_e32 v138, v121, v231
	v_fmac_f32_e32 v137, v122, v231
	v_fmac_f32_e32 v71, v121, v232
	v_fmac_f32_e32 v70, v122, v232
	v_fmac_f32_e32 v69, v121, v233
	v_fmac_f32_e32 v68, v122, v233
	s_waitcnt vmcnt(14)
	v_fmac_f32_e32 v140, v123, v242
	s_waitcnt vmcnt(13)
	v_fmac_f32_e32 v148, v123, v246
	s_waitcnt vmcnt(12)
	v_fmac_f32_e32 v156, v123, v250
	v_fmac_f32_e32 v155, v124, v250
	v_fmac_f32_e32 v154, v123, v251
	v_fmac_f32_e32 v153, v124, v251
	v_fmac_f32_e32 v152, v123, v252
	v_fmac_f32_e32 v151, v124, v252
	v_fmac_f32_e32 v150, v123, v253
	v_fmac_f32_e32 v149, v124, v253
	v_fmac_f32_e32 v147, v124, v246
	v_fmac_f32_e32 v146, v123, v247
	v_fmac_f32_e32 v145, v124, v247
	v_fmac_f32_e32 v144, v123, v248
	v_fmac_f32_e32 v143, v124, v248
	v_fmac_f32_e32 v142, v123, v249
	v_fmac_f32_e32 v141, v124, v249
	v_fmac_f32_e32 v139, v124, v242
	v_fmac_f32_e32 v138, v123, v243
	v_fmac_f32_e32 v137, v124, v243
	v_fmac_f32_e32 v71, v123, v244
	v_fmac_f32_e32 v70, v124, v244
	v_fmac_f32_e32 v69, v123, v245
	v_fmac_f32_e32 v68, v124, v245
	s_waitcnt vmcnt(11)
	v_fmac_f32_e32 v140, v125, v2
	s_waitcnt vmcnt(10)
	v_fmac_f32_e32 v148, v125, v6
	s_waitcnt vmcnt(9)
	v_fmac_f32_e32 v156, v125, v158
	v_fmac_f32_e32 v155, v126, v158
	v_fmac_f32_e32 v154, v125, v159
	v_fmac_f32_e32 v153, v126, v159
	v_fmac_f32_e32 v152, v125, v160
	v_fmac_f32_e32 v151, v126, v160
	v_fmac_f32_e32 v150, v125, v161
	v_fmac_f32_e32 v149, v126, v161
	v_fmac_f32_e32 v147, v126, v6
	v_fmac_f32_e32 v146, v125, v7
	v_fmac_f32_e32 v145, v126, v7
	v_fmac_f32_e32 v144, v125, v8
	v_fmac_f32_e32 v143, v126, v8
	v_fmac_f32_e32 v142, v125, v9
	v_fmac_f32_e32 v141, v126, v9
	v_fmac_f32_e32 v139, v126, v2
	v_fmac_f32_e32 v138, v125, v3
	v_fmac_f32_e32 v137, v126, v3
	v_fmac_f32_e32 v71, v125, v4
	v_fmac_f32_e32 v70, v126, v4
	v_fmac_f32_e32 v69, v125, v5
	v_fmac_f32_e32 v68, v126, v5
	s_waitcnt vmcnt(8)
	v_fmac_f32_e32 v140, v127, v164
	s_waitcnt vmcnt(7)
	v_fmac_f32_e32 v148, v127, v168
	s_waitcnt vmcnt(6)
	v_fmac_f32_e32 v156, v127, v172
	v_fmac_f32_e32 v155, v128, v172
	v_fmac_f32_e32 v154, v127, v173
	v_fmac_f32_e32 v153, v128, v173
	v_fmac_f32_e32 v152, v127, v174
	v_fmac_f32_e32 v151, v128, v174
	v_fmac_f32_e32 v150, v127, v175
	v_fmac_f32_e32 v149, v128, v175
	v_fmac_f32_e32 v147, v128, v168
	v_fmac_f32_e32 v146, v127, v169
	v_fmac_f32_e32 v145, v128, v169
	v_fmac_f32_e32 v144, v127, v170
	v_fmac_f32_e32 v143, v128, v170
	v_fmac_f32_e32 v142, v127, v171
	v_fmac_f32_e32 v141, v128, v171
	v_fmac_f32_e32 v139, v128, v164
	v_fmac_f32_e32 v138, v127, v165
	v_fmac_f32_e32 v137, v128, v165
	v_fmac_f32_e32 v71, v127, v166
	v_fmac_f32_e32 v70, v128, v166
	v_fmac_f32_e32 v69, v127, v167
	v_fmac_f32_e32 v68, v128, v167
	s_waitcnt vmcnt(5)
	v_fmac_f32_e32 v140, v129, v176
	s_waitcnt vmcnt(4)
	v_fmac_f32_e32 v148, v129, v180
	s_waitcnt vmcnt(3)
	v_fmac_f32_e32 v156, v129, v184
	v_fmac_f32_e32 v155, v130, v184
	v_fmac_f32_e32 v154, v129, v185
	v_fmac_f32_e32 v153, v130, v185
	v_fmac_f32_e32 v152, v129, v186
	v_fmac_f32_e32 v151, v130, v186
	v_fmac_f32_e32 v150, v129, v187
	v_fmac_f32_e32 v149, v130, v187
	v_fmac_f32_e32 v147, v130, v180
	v_fmac_f32_e32 v146, v129, v181
	v_fmac_f32_e32 v145, v130, v181
	v_fmac_f32_e32 v144, v129, v182
	v_fmac_f32_e32 v143, v130, v182
	v_fmac_f32_e32 v142, v129, v183
	v_fmac_f32_e32 v141, v130, v183
	v_fmac_f32_e32 v139, v130, v176
	v_fmac_f32_e32 v138, v129, v177
	v_fmac_f32_e32 v137, v130, v177
	v_fmac_f32_e32 v71, v129, v178
	v_fmac_f32_e32 v70, v130, v178
	v_fmac_f32_e32 v69, v129, v179
	v_fmac_f32_e32 v68, v130, v179
	s_waitcnt vmcnt(2)
	v_fmac_f32_e32 v140, v131, v200
	s_waitcnt vmcnt(1)
	v_fmac_f32_e32 v148, v131, v204
	s_waitcnt vmcnt(0)
	v_fmac_f32_e32 v156, v131, v208
	v_fmac_f32_e32 v155, v132, v208
	v_fmac_f32_e32 v154, v131, v209
	v_fmac_f32_e32 v153, v132, v209
	v_fmac_f32_e32 v152, v131, v210
	v_fmac_f32_e32 v151, v132, v210
	v_fmac_f32_e32 v150, v131, v211
	v_fmac_f32_e32 v149, v132, v211
	v_fmac_f32_e32 v147, v132, v204
	v_fmac_f32_e32 v146, v131, v205
	v_fmac_f32_e32 v145, v132, v205
	v_fmac_f32_e32 v144, v131, v206
	v_fmac_f32_e32 v143, v132, v206
	v_fmac_f32_e32 v142, v131, v207
	v_fmac_f32_e32 v141, v132, v207
	v_fmac_f32_e32 v139, v132, v200
	v_fmac_f32_e32 v138, v131, v201
	v_fmac_f32_e32 v137, v132, v201
	v_fmac_f32_e32 v71, v131, v202
	v_fmac_f32_e32 v70, v132, v202
	v_fmac_f32_e32 v69, v131, v203
	v_fmac_f32_e32 v68, v132, v203
	v_lshl_add_u64 v[10:11], v[0:1], 0, v[64:65]
	global_load_dwordx4 v[2:5], v[10:11], off offset:32
	global_load_dwordx4 v[6:9], v[10:11], off offset:16
	global_load_dwordx4 v[158:161], v[10:11], off
	s_waitcnt vmcnt(2)
	v_fmac_f32_e32 v140, v133, v2
	s_waitcnt vmcnt(1)
	v_fmac_f32_e32 v144, v133, v8
	v_fmac_f32_e32 v143, v134, v8
	v_fmac_f32_e32 v142, v133, v9
	v_fmac_f32_e32 v141, v134, v9
	v_lshl_add_u64 v[8:9], v[0:1], 0, v[66:67]
	v_fmac_f32_e32 v148, v133, v6
	v_fmac_f32_e32 v147, v134, v6
	v_fmac_f32_e32 v146, v133, v7
	v_fmac_f32_e32 v145, v134, v7
	v_fmac_f32_e32 v139, v134, v2
	v_fmac_f32_e32 v138, v133, v3
	v_fmac_f32_e32 v137, v134, v3
	v_fmac_f32_e32 v71, v133, v4
	v_fmac_f32_e32 v70, v134, v4
	v_fmac_f32_e32 v69, v133, v5
	v_fmac_f32_e32 v68, v134, v5
	global_load_dwordx4 v[0:3], v[8:9], off offset:32
	global_load_dwordx4 v[4:7], v[8:9], off offset:16
	s_nop 0
	global_load_dwordx4 v[8:11], v[8:9], off
	s_waitcnt vmcnt(3)
	v_fmac_f32_e32 v156, v133, v158
	v_fmac_f32_e32 v155, v134, v158
	v_fmac_f32_e32 v154, v133, v159
	v_fmac_f32_e32 v153, v134, v159
	v_fmac_f32_e32 v152, v133, v160
	v_fmac_f32_e32 v151, v134, v160
	v_fmac_f32_e32 v150, v133, v161
	v_fmac_f32_e32 v149, v134, v161
	s_waitcnt vmcnt(2)
	v_fmac_f32_e32 v140, v135, v0
	v_fmac_f32_e32 v139, v136, v0
	s_waitcnt vmcnt(0)
	v_fmac_f32_e32 v156, v135, v8
	v_fmac_f32_e32 v138, v135, v1
	v_fmac_f32_e32 v137, v136, v1
	v_add_f32_dpp v0, v156, v156 quad_perm:[1,0,3,2] row_mask:0xf bank_mask:0xf bound_ctrl:1
	v_fmac_f32_e32 v155, v136, v8
	v_fmac_f32_e32 v154, v135, v9
	v_add_f32_dpp v0, v0, v0 quad_perm:[2,3,0,1] row_mask:0xf bank_mask:0xf bound_ctrl:1
	v_fmac_f32_e32 v153, v136, v9
	v_fmac_f32_e32 v152, v135, v10
	v_add_f32_dpp v0, v0, v0 row_half_mirror row_mask:0xf bank_mask:0xf bound_ctrl:1
	v_fmac_f32_e32 v151, v136, v10
	v_fmac_f32_e32 v150, v135, v11
	v_add_f32_dpp v0, v0, v0 row_mirror row_mask:0xf bank_mask:0xf bound_ctrl:1
	ds_swizzle_b32 v1, v0 offset:swizzle(SWAP,16)
	v_fmac_f32_e32 v149, v136, v11
	v_fmac_f32_e32 v148, v135, v4
	v_fmac_f32_e32 v147, v136, v4
	v_fmac_f32_e32 v146, v135, v5
	s_waitcnt lgkmcnt(0)
	v_add_f32_e32 v0, v0, v1
	v_fmac_f32_e32 v145, v136, v5
	v_readlane_b32 s26, v0, 0
	v_readlane_b32 s27, v0, 32
	v_add_f32_dpp v0, v155, v155 quad_perm:[1,0,3,2] row_mask:0xf bank_mask:0xf bound_ctrl:1
	v_fmac_f32_e32 v144, v135, v6
	v_fmac_f32_e32 v143, v136, v6
	v_add_f32_dpp v0, v0, v0 quad_perm:[2,3,0,1] row_mask:0xf bank_mask:0xf bound_ctrl:1
	v_fmac_f32_e32 v142, v135, v7
	v_fmac_f32_e32 v141, v136, v7
	v_add_f32_dpp v0, v0, v0 row_half_mirror row_mask:0xf bank_mask:0xf bound_ctrl:1
	v_fmac_f32_e32 v71, v135, v2
	v_fmac_f32_e32 v70, v136, v2
	v_add_f32_dpp v0, v0, v0 row_mirror row_mask:0xf bank_mask:0xf bound_ctrl:1
	ds_swizzle_b32 v1, v0 offset:swizzle(SWAP,16)
	v_fmac_f32_e32 v69, v135, v3
	v_fmac_f32_e32 v68, v136, v3
	s_waitcnt lgkmcnt(0)
	v_add_f32_e32 v0, v0, v1
	s_nop 0
	v_readlane_b32 s0, v0, 0
	v_readlane_b32 s28, v0, 32
	v_add_f32_dpp v0, v154, v154 quad_perm:[1,0,3,2] row_mask:0xf bank_mask:0xf bound_ctrl:1
	s_nop 1
	v_add_f32_dpp v0, v0, v0 quad_perm:[2,3,0,1] row_mask:0xf bank_mask:0xf bound_ctrl:1
	s_nop 1
	v_add_f32_dpp v0, v0, v0 row_half_mirror row_mask:0xf bank_mask:0xf bound_ctrl:1
	s_nop 1
	v_add_f32_dpp v0, v0, v0 row_mirror row_mask:0xf bank_mask:0xf bound_ctrl:1
	ds_swizzle_b32 v1, v0 offset:swizzle(SWAP,16)
	s_waitcnt lgkmcnt(0)
	v_add_f32_e32 v0, v0, v1
	s_nop 0
	v_readlane_b32 s29, v0, 0
	v_readlane_b32 s30, v0, 32
	v_add_f32_dpp v0, v153, v153 quad_perm:[1,0,3,2] row_mask:0xf bank_mask:0xf bound_ctrl:1
	s_nop 1
	v_add_f32_dpp v0, v0, v0 quad_perm:[2,3,0,1] row_mask:0xf bank_mask:0xf bound_ctrl:1
	s_nop 1
	v_add_f32_dpp v0, v0, v0 row_half_mirror row_mask:0xf bank_mask:0xf bound_ctrl:1
	s_nop 1
	v_add_f32_dpp v0, v0, v0 row_mirror row_mask:0xf bank_mask:0xf bound_ctrl:1
	ds_swizzle_b32 v1, v0 offset:swizzle(SWAP,16)
	s_waitcnt lgkmcnt(0)
	v_add_f32_e32 v0, v0, v1
	s_nop 0
	v_readlane_b32 s1, v0, 0
	v_readlane_b32 s31, v0, 32
	v_add_f32_dpp v0, v152, v152 quad_perm:[1,0,3,2] row_mask:0xf bank_mask:0xf bound_ctrl:1
	s_nop 1
	v_add_f32_dpp v0, v0, v0 quad_perm:[2,3,0,1] row_mask:0xf bank_mask:0xf bound_ctrl:1
	s_nop 1
	v_add_f32_dpp v0, v0, v0 row_half_mirror row_mask:0xf bank_mask:0xf bound_ctrl:1
	s_nop 1
	v_add_f32_dpp v0, v0, v0 row_mirror row_mask:0xf bank_mask:0xf bound_ctrl:1
	ds_swizzle_b32 v1, v0 offset:swizzle(SWAP,16)
	s_waitcnt lgkmcnt(0)
	v_add_f32_e32 v0, v0, v1
	s_nop 0
	v_readlane_b32 s34, v0, 0
	v_readlane_b32 s35, v0, 32
	v_add_f32_dpp v0, v151, v151 quad_perm:[1,0,3,2] row_mask:0xf bank_mask:0xf bound_ctrl:1
	s_nop 1
	v_add_f32_dpp v0, v0, v0 quad_perm:[2,3,0,1] row_mask:0xf bank_mask:0xf bound_ctrl:1
	s_nop 1
	v_add_f32_dpp v0, v0, v0 row_half_mirror row_mask:0xf bank_mask:0xf bound_ctrl:1
	s_nop 1
	v_add_f32_dpp v0, v0, v0 row_mirror row_mask:0xf bank_mask:0xf bound_ctrl:1
	ds_swizzle_b32 v1, v0 offset:swizzle(SWAP,16)
	s_waitcnt lgkmcnt(0)
	v_add_f32_e32 v0, v0, v1
	s_nop 0
	v_readlane_b32 s14, v0, 0
	v_readlane_b32 s36, v0, 32
	v_add_f32_dpp v0, v150, v150 quad_perm:[1,0,3,2] row_mask:0xf bank_mask:0xf bound_ctrl:1
	s_nop 1
	v_add_f32_dpp v0, v0, v0 quad_perm:[2,3,0,1] row_mask:0xf bank_mask:0xf bound_ctrl:1
	s_nop 1
	v_add_f32_dpp v0, v0, v0 row_half_mirror row_mask:0xf bank_mask:0xf bound_ctrl:1
	s_nop 1
	v_add_f32_dpp v0, v0, v0 row_mirror row_mask:0xf bank_mask:0xf bound_ctrl:1
	ds_swizzle_b32 v1, v0 offset:swizzle(SWAP,16)
	s_waitcnt lgkmcnt(0)
	v_add_f32_e32 v0, v0, v1
	s_nop 0
	v_readlane_b32 s37, v0, 0
	v_readlane_b32 s38, v0, 32
	v_add_f32_dpp v0, v149, v149 quad_perm:[1,0,3,2] row_mask:0xf bank_mask:0xf bound_ctrl:1
	s_nop 1
	v_add_f32_dpp v0, v0, v0 quad_perm:[2,3,0,1] row_mask:0xf bank_mask:0xf bound_ctrl:1
	s_nop 1
	v_add_f32_dpp v0, v0, v0 row_half_mirror row_mask:0xf bank_mask:0xf bound_ctrl:1
	s_nop 1
	v_add_f32_dpp v0, v0, v0 row_mirror row_mask:0xf bank_mask:0xf bound_ctrl:1
	ds_swizzle_b32 v1, v0 offset:swizzle(SWAP,16)
	s_waitcnt lgkmcnt(0)
	v_add_f32_e32 v0, v0, v1
	s_nop 0
	v_readlane_b32 s15, v0, 0
	v_readlane_b32 s39, v0, 32
	v_add_f32_dpp v0, v148, v148 quad_perm:[1,0,3,2] row_mask:0xf bank_mask:0xf bound_ctrl:1
	s_nop 1
	v_add_f32_dpp v0, v0, v0 quad_perm:[2,3,0,1] row_mask:0xf bank_mask:0xf bound_ctrl:1
	s_nop 1
	v_add_f32_dpp v0, v0, v0 row_half_mirror row_mask:0xf bank_mask:0xf bound_ctrl:1
	s_nop 1
	v_add_f32_dpp v0, v0, v0 row_mirror row_mask:0xf bank_mask:0xf bound_ctrl:1
	ds_swizzle_b32 v1, v0 offset:swizzle(SWAP,16)
	s_waitcnt lgkmcnt(0)
	v_add_f32_e32 v0, v0, v1
	s_nop 0
	v_readlane_b32 s40, v0, 0
	v_readlane_b32 s41, v0, 32
	v_add_f32_dpp v0, v147, v147 quad_perm:[1,0,3,2] row_mask:0xf bank_mask:0xf bound_ctrl:1
	s_nop 1
	v_add_f32_dpp v0, v0, v0 quad_perm:[2,3,0,1] row_mask:0xf bank_mask:0xf bound_ctrl:1
	s_nop 1
	v_add_f32_dpp v0, v0, v0 row_half_mirror row_mask:0xf bank_mask:0xf bound_ctrl:1
	s_nop 1
	v_add_f32_dpp v0, v0, v0 row_mirror row_mask:0xf bank_mask:0xf bound_ctrl:1
	ds_swizzle_b32 v1, v0 offset:swizzle(SWAP,16)
	s_waitcnt lgkmcnt(0)
	v_add_f32_e32 v0, v0, v1
	s_nop 0
	v_readlane_b32 s12, v0, 0
	v_readlane_b32 s42, v0, 32
	v_add_f32_dpp v0, v146, v146 quad_perm:[1,0,3,2] row_mask:0xf bank_mask:0xf bound_ctrl:1
	s_nop 1
	v_add_f32_dpp v0, v0, v0 quad_perm:[2,3,0,1] row_mask:0xf bank_mask:0xf bound_ctrl:1
	s_nop 1
	v_add_f32_dpp v0, v0, v0 row_half_mirror row_mask:0xf bank_mask:0xf bound_ctrl:1
	s_nop 1
	v_add_f32_dpp v0, v0, v0 row_mirror row_mask:0xf bank_mask:0xf bound_ctrl:1
	ds_swizzle_b32 v1, v0 offset:swizzle(SWAP,16)
	s_waitcnt lgkmcnt(0)
	v_add_f32_e32 v0, v0, v1
	s_nop 0
	v_readlane_b32 s43, v0, 0
	v_readlane_b32 s44, v0, 32
	v_add_f32_dpp v0, v145, v145 quad_perm:[1,0,3,2] row_mask:0xf bank_mask:0xf bound_ctrl:1
	s_nop 1
	v_add_f32_dpp v0, v0, v0 quad_perm:[2,3,0,1] row_mask:0xf bank_mask:0xf bound_ctrl:1
	s_nop 1
	v_add_f32_dpp v0, v0, v0 row_half_mirror row_mask:0xf bank_mask:0xf bound_ctrl:1
	s_nop 1
	v_add_f32_dpp v0, v0, v0 row_mirror row_mask:0xf bank_mask:0xf bound_ctrl:1
	ds_swizzle_b32 v1, v0 offset:swizzle(SWAP,16)
	s_waitcnt lgkmcnt(0)
	v_add_f32_e32 v0, v0, v1
	s_nop 0
	v_readlane_b32 s13, v0, 0
	v_readlane_b32 s45, v0, 32
	v_add_f32_dpp v0, v144, v144 quad_perm:[1,0,3,2] row_mask:0xf bank_mask:0xf bound_ctrl:1
	s_nop 1
	v_add_f32_dpp v0, v0, v0 quad_perm:[2,3,0,1] row_mask:0xf bank_mask:0xf bound_ctrl:1
	s_nop 1
	v_add_f32_dpp v0, v0, v0 row_half_mirror row_mask:0xf bank_mask:0xf bound_ctrl:1
	s_nop 1
	v_add_f32_dpp v0, v0, v0 row_mirror row_mask:0xf bank_mask:0xf bound_ctrl:1
	ds_swizzle_b32 v1, v0 offset:swizzle(SWAP,16)
	s_waitcnt lgkmcnt(0)
	v_add_f32_e32 v0, v0, v1
	s_nop 0
	v_readlane_b32 s46, v0, 0
	v_readlane_b32 s47, v0, 32
	v_add_f32_dpp v0, v143, v143 quad_perm:[1,0,3,2] row_mask:0xf bank_mask:0xf bound_ctrl:1
	s_nop 1
	v_add_f32_dpp v0, v0, v0 quad_perm:[2,3,0,1] row_mask:0xf bank_mask:0xf bound_ctrl:1
	s_nop 1
	v_add_f32_dpp v0, v0, v0 row_half_mirror row_mask:0xf bank_mask:0xf bound_ctrl:1
	s_nop 1
	v_add_f32_dpp v0, v0, v0 row_mirror row_mask:0xf bank_mask:0xf bound_ctrl:1
	ds_swizzle_b32 v1, v0 offset:swizzle(SWAP,16)
	s_waitcnt lgkmcnt(0)
	v_add_f32_e32 v0, v0, v1
	s_nop 0
	v_readlane_b32 s16, v0, 0
	v_readlane_b32 s48, v0, 32
	v_add_f32_dpp v0, v142, v142 quad_perm:[1,0,3,2] row_mask:0xf bank_mask:0xf bound_ctrl:1
	s_nop 1
	v_add_f32_dpp v0, v0, v0 quad_perm:[2,3,0,1] row_mask:0xf bank_mask:0xf bound_ctrl:1
	s_nop 1
	v_add_f32_dpp v0, v0, v0 row_half_mirror row_mask:0xf bank_mask:0xf bound_ctrl:1
	s_nop 1
	v_add_f32_dpp v0, v0, v0 row_mirror row_mask:0xf bank_mask:0xf bound_ctrl:1
	ds_swizzle_b32 v1, v0 offset:swizzle(SWAP,16)
	s_waitcnt lgkmcnt(0)
	v_add_f32_e32 v0, v0, v1
	s_nop 0
	v_readlane_b32 s49, v0, 0
	v_readlane_b32 s50, v0, 32
	v_add_f32_dpp v0, v141, v141 quad_perm:[1,0,3,2] row_mask:0xf bank_mask:0xf bound_ctrl:1
	s_nop 1
	v_add_f32_dpp v0, v0, v0 quad_perm:[2,3,0,1] row_mask:0xf bank_mask:0xf bound_ctrl:1
	s_nop 1
	v_add_f32_dpp v0, v0, v0 row_half_mirror row_mask:0xf bank_mask:0xf bound_ctrl:1
	s_nop 1
	v_add_f32_dpp v0, v0, v0 row_mirror row_mask:0xf bank_mask:0xf bound_ctrl:1
	ds_swizzle_b32 v1, v0 offset:swizzle(SWAP,16)
	s_waitcnt lgkmcnt(0)
	v_add_f32_e32 v0, v0, v1
	s_nop 0
	v_readlane_b32 s17, v0, 0
	v_readlane_b32 s51, v0, 32
	v_add_f32_dpp v0, v140, v140 quad_perm:[1,0,3,2] row_mask:0xf bank_mask:0xf bound_ctrl:1
	s_nop 1
	v_add_f32_dpp v0, v0, v0 quad_perm:[2,3,0,1] row_mask:0xf bank_mask:0xf bound_ctrl:1
	s_nop 1
	v_add_f32_dpp v0, v0, v0 row_half_mirror row_mask:0xf bank_mask:0xf bound_ctrl:1
	s_nop 1
	v_add_f32_dpp v0, v0, v0 row_mirror row_mask:0xf bank_mask:0xf bound_ctrl:1
	ds_swizzle_b32 v1, v0 offset:swizzle(SWAP,16)
	s_waitcnt lgkmcnt(0)
	v_add_f32_e32 v0, v0, v1
	s_nop 0
	v_readlane_b32 s52, v0, 0
	v_readlane_b32 s53, v0, 32
	v_add_f32_dpp v0, v139, v139 quad_perm:[1,0,3,2] row_mask:0xf bank_mask:0xf bound_ctrl:1
	s_nop 1
	v_add_f32_dpp v0, v0, v0 quad_perm:[2,3,0,1] row_mask:0xf bank_mask:0xf bound_ctrl:1
	s_nop 1
	v_add_f32_dpp v0, v0, v0 row_half_mirror row_mask:0xf bank_mask:0xf bound_ctrl:1
	s_nop 1
	v_add_f32_dpp v0, v0, v0 row_mirror row_mask:0xf bank_mask:0xf bound_ctrl:1
	ds_swizzle_b32 v1, v0 offset:swizzle(SWAP,16)
	s_waitcnt lgkmcnt(0)
	v_add_f32_e32 v0, v0, v1
	s_nop 0
	v_readlane_b32 s18, v0, 0
	v_readlane_b32 s54, v0, 32
	v_add_f32_dpp v0, v138, v138 quad_perm:[1,0,3,2] row_mask:0xf bank_mask:0xf bound_ctrl:1
	s_nop 1
	v_add_f32_dpp v0, v0, v0 quad_perm:[2,3,0,1] row_mask:0xf bank_mask:0xf bound_ctrl:1
	s_nop 1
	v_add_f32_dpp v0, v0, v0 row_half_mirror row_mask:0xf bank_mask:0xf bound_ctrl:1
	s_nop 1
	v_add_f32_dpp v0, v0, v0 row_mirror row_mask:0xf bank_mask:0xf bound_ctrl:1
	ds_swizzle_b32 v1, v0 offset:swizzle(SWAP,16)
	s_waitcnt lgkmcnt(0)
	v_add_f32_e32 v0, v0, v1
	s_nop 0
	v_readlane_b32 s55, v0, 0
	v_readlane_b32 s56, v0, 32
	v_add_f32_dpp v0, v137, v137 quad_perm:[1,0,3,2] row_mask:0xf bank_mask:0xf bound_ctrl:1
	s_nop 1
	v_add_f32_dpp v0, v0, v0 quad_perm:[2,3,0,1] row_mask:0xf bank_mask:0xf bound_ctrl:1
	s_nop 1
	v_add_f32_dpp v0, v0, v0 row_half_mirror row_mask:0xf bank_mask:0xf bound_ctrl:1
	s_nop 1
	v_add_f32_dpp v0, v0, v0 row_mirror row_mask:0xf bank_mask:0xf bound_ctrl:1
	ds_swizzle_b32 v1, v0 offset:swizzle(SWAP,16)
	s_waitcnt lgkmcnt(0)
	v_add_f32_e32 v0, v0, v1
	s_nop 0
	v_readlane_b32 s19, v0, 0
	v_readlane_b32 s57, v0, 32
	v_add_f32_dpp v0, v71, v71 quad_perm:[1,0,3,2] row_mask:0xf bank_mask:0xf bound_ctrl:1
	s_nop 1
	v_add_f32_dpp v0, v0, v0 quad_perm:[2,3,0,1] row_mask:0xf bank_mask:0xf bound_ctrl:1
	s_nop 1
	v_add_f32_dpp v0, v0, v0 row_half_mirror row_mask:0xf bank_mask:0xf bound_ctrl:1
	s_nop 1
	v_add_f32_dpp v0, v0, v0 row_mirror row_mask:0xf bank_mask:0xf bound_ctrl:1
	ds_swizzle_b32 v1, v0 offset:swizzle(SWAP,16)
	s_waitcnt lgkmcnt(0)
	v_add_f32_e32 v0, v0, v1
	s_nop 0
	v_readlane_b32 s58, v0, 0
	v_readlane_b32 s59, v0, 32
	v_add_f32_dpp v0, v70, v70 quad_perm:[1,0,3,2] row_mask:0xf bank_mask:0xf bound_ctrl:1
	s_nop 1
	v_add_f32_dpp v0, v0, v0 quad_perm:[2,3,0,1] row_mask:0xf bank_mask:0xf bound_ctrl:1
	s_nop 1
	v_add_f32_dpp v0, v0, v0 row_half_mirror row_mask:0xf bank_mask:0xf bound_ctrl:1
	s_nop 1
	v_add_f32_dpp v0, v0, v0 row_mirror row_mask:0xf bank_mask:0xf bound_ctrl:1
	ds_swizzle_b32 v1, v0 offset:swizzle(SWAP,16)
	s_waitcnt lgkmcnt(0)
	v_add_f32_e32 v0, v0, v1
	s_nop 0
	v_readlane_b32 s22, v0, 0
	v_readlane_b32 s60, v0, 32
	v_add_f32_dpp v0, v69, v69 quad_perm:[1,0,3,2] row_mask:0xf bank_mask:0xf bound_ctrl:1
	s_nop 1
	v_add_f32_dpp v0, v0, v0 quad_perm:[2,3,0,1] row_mask:0xf bank_mask:0xf bound_ctrl:1
	s_nop 1
	v_add_f32_dpp v0, v0, v0 row_half_mirror row_mask:0xf bank_mask:0xf bound_ctrl:1
	s_nop 1
	v_add_f32_dpp v0, v0, v0 row_mirror row_mask:0xf bank_mask:0xf bound_ctrl:1
	ds_swizzle_b32 v1, v0 offset:swizzle(SWAP,16)
	s_waitcnt lgkmcnt(0)
	v_add_f32_e32 v0, v0, v1
	s_nop 0
	v_readlane_b32 s61, v0, 0
	v_readlane_b32 s62, v0, 32
	v_add_f32_dpp v0, v68, v68 quad_perm:[1,0,3,2] row_mask:0xf bank_mask:0xf bound_ctrl:1
	s_nop 1
	v_add_f32_dpp v0, v0, v0 quad_perm:[2,3,0,1] row_mask:0xf bank_mask:0xf bound_ctrl:1
	s_nop 1
	v_add_f32_dpp v0, v0, v0 row_half_mirror row_mask:0xf bank_mask:0xf bound_ctrl:1
	s_nop 1
	v_add_f32_dpp v0, v0, v0 row_mirror row_mask:0xf bank_mask:0xf bound_ctrl:1
	ds_swizzle_b32 v1, v0 offset:swizzle(SWAP,16)
	s_waitcnt lgkmcnt(0)
	v_add_f32_e32 v0, v0, v1
	s_nop 0
	v_readlane_b32 s23, v0, 0
	v_readlane_b32 s63, v0, 32
	s_and_saveexec_b64 s[20:21], vcc
	s_cbranch_execz .LBB0_1025
	v_lshlrev_b64 v[68:69], 2, v[12:13]
	v_lshl_add_u64 v[140:141], s[6:7], 0, v[68:69]
	v_lshl_add_u64 v[70:71], s[8:9], 0, v[68:69]
	v_add_u32_e32 v68, 1, v12
	v_ashrrev_i32_e32 v69, 31, v68
	v_lshlrev_b64 v[68:69], 2, v[68:69]
	global_load_dword v138, v[140:141], off
	v_lshl_add_u64 v[142:143], s[6:7], 0, v[68:69]
	global_load_dword v139, v[142:143], off
	v_mov_b32_e32 v2, s38
	v_mov_b32_e32 v37, s27
	v_add_f32_e32 v31, s37, v2
	v_mov_b32_e32 v2, s35
	v_mov_b32_e32 v35, s30
	v_add_f32_e32 v37, s26, v37
	v_add_f32_e32 v33, s34, v2
	v_mov_b32_e32 v2, s28
	v_mov_b32_e32 v3, s31
	v_add_f32_e32 v35, s29, v35
	v_lshl_add_u64 v[68:69], s[8:9], 0, v[68:69]
	v_pk_add_f32 v[2:3], s[0:1], v[2:3]
	s_mov_b32 s0, 0xc000
	v_mov_b32_e32 v0, s62
	v_add_f32_e32 v15, s61, v0
	v_mov_b32_e32 v0, s59
	v_add_f32_e32 v17, s58, v0
	v_mov_b32_e32 v0, s56
	v_add_f32_e32 v19, s55, v0
	v_mov_b32_e32 v0, s53
	v_add_f32_e32 v21, s52, v0
	v_mov_b32_e32 v0, s50
	v_add_f32_e32 v23, s49, v0
	v_mov_b32_e32 v0, s47
	v_add_f32_e32 v25, s46, v0
	v_mov_b32_e32 v0, s44
	v_add_f32_e32 v27, s43, v0
	v_mov_b32_e32 v0, s41
	v_add_f32_e32 v29, s40, v0
	v_mov_b32_e32 v0, s36
	v_mov_b32_e32 v1, s39
	v_pk_add_f32 v[0:1], s[14:15], v[0:1]
	v_mov_b32_e32 v10, s42
	v_mov_b32_e32 v11, s45
	v_mov_b32_e32 v6, s54
	v_mov_b32_e32 v7, s57
	v_pk_add_f32 v[10:11], s[12:13], v[10:11]
	v_mov_b32_e32 v4, s60
	v_mov_b32_e32 v5, s63
	v_mov_b32_e32 v8, s48
	v_mov_b32_e32 v9, s51
	v_pk_add_f32 v[6:7], s[18:19], v[6:7]
	v_pk_add_f32 v[8:9], s[16:17], v[8:9]
	s_waitcnt vmcnt(1)
	v_add_f32_e32 v13, v37, v138
	global_store_dword v[70:71], v13, off
	s_waitcnt vmcnt(1)
	v_add_f32_e32 v13, v35, v139
	global_store_dword v[68:69], v13, off
	v_add_co_u32_e64 v68, s[0:1], s0, v70
	v_pk_add_f32 v[2:3], v[2:3], v[138:139]
	s_nop 0
	v_addc_co_u32_e64 v69, s[0:1], 0, v71, s[0:1]
	global_store_dwordx2 v[68:69], v[2:3], off
	v_add_u32_e32 v2, 2, v12
	v_ashrrev_i32_e32 v3, 31, v2
	v_lshlrev_b64 v[2:3], 2, v[2:3]
	v_lshl_add_u64 v[138:139], s[6:7], 0, v[2:3]
	global_load_dword v138, v[138:139], off
	v_lshl_add_u64 v[2:3], s[8:9], 0, v[2:3]
	s_waitcnt vmcnt(0)
	v_add_f32_e32 v13, v33, v138
	global_store_dword v[2:3], v13, off
	v_add_u32_e32 v2, 3, v12
	v_ashrrev_i32_e32 v3, 31, v2
	v_lshlrev_b64 v[2:3], 2, v[2:3]
	v_lshl_add_u64 v[142:143], s[6:7], 0, v[2:3]
	global_load_dword v139, v[142:143], off
	v_lshl_add_u64 v[2:3], s[8:9], 0, v[2:3]
	s_waitcnt vmcnt(0)
	v_add_f32_e32 v13, v31, v139
	global_store_dword v[2:3], v13, off
	v_pk_add_f32 v[138:139], v[0:1], v[138:139]
	global_load_dwordx4 v[0:3], v[140:141], off offset:32
	s_nop 0
	global_load_dwordx4 v[140:143], v[140:141], off offset:16
	s_waitcnt vmcnt(0)
	v_add_f32_e32 v144, v29, v140
	v_add_f32_e32 v145, v27, v141
	v_pk_add_f32 v[140:141], v[10:11], v[140:141]
	global_store_dwordx4 v[68:69], v[138:141], off offset:8
	v_pk_add_f32 v[10:11], v[6:7], v[0:1]
	v_add_f32_e32 v146, v25, v142
	v_add_f32_e32 v138, v21, v0
	v_add_f32_e32 v139, v19, v1
	v_pk_add_f32 v[0:1], s[22:23], v[4:5]
	v_add_f32_e32 v147, v23, v143
	v_pk_add_f32 v[8:9], v[8:9], v[142:143]
	v_add_f32_e32 v140, v17, v2
	v_add_f32_e32 v141, v15, v3
	v_pk_add_f32 v[0:1], v[0:1], v[2:3]
	global_store_dwordx4 v[70:71], v[144:147], off offset:16
	global_store_dwordx4 v[68:69], v[8:11], off offset:24
	global_store_dwordx4 v[70:71], v[138:141], off offset:32
	global_store_dwordx2 v[68:69], v[0:1], off offset:40
	s_branch .LBB0_1025
